# prologue/epilogue de-serialisation: kernel-argument loads of the spmm kernels hoisted to kernel entry (fresh SGPRs), rowptr pointer load issued with the first argument loads
# speedup vs baseline: 1.0695x; 1.0004x over previous
_Z6k_spmmILb0ELi0EEvPKiPK15HIP_vector_typeIiLj2EEPKvPKfPKDF16_S9_S9_iPfPDF16_PhSC_PKhS9_SG_S9_S9_i:
	s_load_dword s3, s[0:1], 0x90
	s_load_dwordx2 s[40:41], s[0:1], 0x10
	s_load_dwordx4 s[44:47], s[0:1], 0x48
	s_load_dwordx2 s[48:49], s[0:1], 0x20
	s_load_dwordx2 s[8:9], s[0:1], 0x0
	s_load_dwordx2 s[6:7], s[0:1], 0x8
	s_load_dword s4, s[0:1], 0x38
	v_lshrrev_b32_e32 v1, 4, v0
	s_waitcnt lgkmcnt(0)
	s_lshr_b32 s13, s3, 12
	s_lshl_b32 s13, s13, 12
	s_cmp_lt_u32 s2, s13
	s_cbranch_scc0 .Lperm_skip0
	s_and_b32 s14, s2, 511
	s_lshr_b32 s15, s2, 9
	s_lshr_b32 s16, s15, 2
	s_and_b32 s17, s15, 1
	s_bfe_u32 s15, s15, 0x10001
	s_lshl_b32 s16, s16, 1
	s_add_i32 s16, s16, s17
	s_lshl_b32 s16, s16, 10
	s_lshl_b32 s15, s15, 9
	s_or_b32 s2, s16, s15
	s_or_b32 s2, s2, s14
.Lperm_skip0:
	s_not_b32 s2, s2
	s_add_i32 s12, s3, s2
	v_bfe_u32 v2, v0, 4, 2
	s_lshl_b32 s2, s12, 5
	v_and_b32_e32 v3, 28, v1
	s_nop 0
	v_mbcnt_lo_u32_b32 v5, -1, 0
	v_mbcnt_hi_u32_b32 v5, -1, v5
	v_min_u32_e32 v6, 32, v5
	v_add_u32_e32 v6, s2, v6
	v_min_i32_e32 v6, s4, v6
	v_lshlrev_b32_e32 v7, 2, v6
	v_lshrrev_b32_e32 v9, 6, v0
	v_lshlrev_b32_e32 v9, 9, v9
	v_lshlrev_b32_e32 v10, 2, v5
	v_add_u32_e32 v11, v9, v10
	s_waitcnt lgkmcnt(0)
	global_load_dword v8, v7, s[8:9]
	v_cmp_gt_u32_e32 vcc, 33, v5
	s_waitcnt vmcnt(0)
	s_and_saveexec_b64 s[10:11], vcc
	ds_write_b32 v11, v8 offset:16448
	s_mov_b64 exec, s[10:11]
	ds_read_b32 v12, v11 offset:16452
	v_sub_u32_e32 v13, 31, v5
	s_waitcnt lgkmcnt(0)
	v_sub_u32_e32 v12, v12, v8
	v_lshl_add_u32 v12, v12, 5, v13
	v_cmp_gt_u32_e32 vcc, 32, v5
	s_and_saveexec_b64 s[10:11], vcc
	ds_write_b32 v11, v12 offset:16608
	s_mov_b64 exec, s[10:11]
	v_mov_b32_e32 v13, 0
	ds_read_b128 v[14:17], v9 offset:16608
	s_waitcnt lgkmcnt(0)
	v_sub_u32_e32 v6, v12, v14
	v_ashrrev_i32_e32 v6, 31, v6
	v_sub_u32_e32 v13, v13, v6
	v_sub_u32_e32 v6, v12, v15
	v_ashrrev_i32_e32 v6, 31, v6
	v_sub_u32_e32 v13, v13, v6
	v_sub_u32_e32 v6, v12, v16
	v_ashrrev_i32_e32 v6, 31, v6
	v_sub_u32_e32 v13, v13, v6
	v_sub_u32_e32 v6, v12, v17
	v_ashrrev_i32_e32 v6, 31, v6
	v_sub_u32_e32 v13, v13, v6
	ds_read_b128 v[14:17], v9 offset:16624
	s_waitcnt lgkmcnt(0)
	v_sub_u32_e32 v6, v12, v14
	v_ashrrev_i32_e32 v6, 31, v6
	v_sub_u32_e32 v13, v13, v6
	v_sub_u32_e32 v6, v12, v15
	v_ashrrev_i32_e32 v6, 31, v6
	v_sub_u32_e32 v13, v13, v6
	v_sub_u32_e32 v6, v12, v16
	v_ashrrev_i32_e32 v6, 31, v6
	v_sub_u32_e32 v13, v13, v6
	v_sub_u32_e32 v6, v12, v17
	v_ashrrev_i32_e32 v6, 31, v6
	v_sub_u32_e32 v13, v13, v6
	ds_read_b128 v[14:17], v9 offset:16640
	s_waitcnt lgkmcnt(0)
	v_sub_u32_e32 v6, v12, v14
	v_ashrrev_i32_e32 v6, 31, v6
	v_sub_u32_e32 v13, v13, v6
	v_sub_u32_e32 v6, v12, v15
	v_ashrrev_i32_e32 v6, 31, v6
	v_sub_u32_e32 v13, v13, v6
	v_sub_u32_e32 v6, v12, v16
	v_ashrrev_i32_e32 v6, 31, v6
	v_sub_u32_e32 v13, v13, v6
	v_sub_u32_e32 v6, v12, v17
	v_ashrrev_i32_e32 v6, 31, v6
	v_sub_u32_e32 v13, v13, v6
	ds_read_b128 v[14:17], v9 offset:16656
	s_waitcnt lgkmcnt(0)
	v_sub_u32_e32 v6, v12, v14
	v_ashrrev_i32_e32 v6, 31, v6
	v_sub_u32_e32 v13, v13, v6
	v_sub_u32_e32 v6, v12, v15
	v_ashrrev_i32_e32 v6, 31, v6
	v_sub_u32_e32 v13, v13, v6
	v_sub_u32_e32 v6, v12, v16
	v_ashrrev_i32_e32 v6, 31, v6
	v_sub_u32_e32 v13, v13, v6
	v_sub_u32_e32 v6, v12, v17
	v_ashrrev_i32_e32 v6, 31, v6
	v_sub_u32_e32 v13, v13, v6
	ds_read_b128 v[14:17], v9 offset:16672
	s_waitcnt lgkmcnt(0)
	v_sub_u32_e32 v6, v12, v14
	v_ashrrev_i32_e32 v6, 31, v6
	v_sub_u32_e32 v13, v13, v6
	v_sub_u32_e32 v6, v12, v15
	v_ashrrev_i32_e32 v6, 31, v6
	v_sub_u32_e32 v13, v13, v6
	v_sub_u32_e32 v6, v12, v16
	v_ashrrev_i32_e32 v6, 31, v6
	v_sub_u32_e32 v13, v13, v6
	v_sub_u32_e32 v6, v12, v17
	v_ashrrev_i32_e32 v6, 31, v6
	v_sub_u32_e32 v13, v13, v6
	ds_read_b128 v[14:17], v9 offset:16688
	s_waitcnt lgkmcnt(0)
	v_sub_u32_e32 v6, v12, v14
	v_ashrrev_i32_e32 v6, 31, v6
	v_sub_u32_e32 v13, v13, v6
	v_sub_u32_e32 v6, v12, v15
	v_ashrrev_i32_e32 v6, 31, v6
	v_sub_u32_e32 v13, v13, v6
	v_sub_u32_e32 v6, v12, v16
	v_ashrrev_i32_e32 v6, 31, v6
	v_sub_u32_e32 v13, v13, v6
	v_sub_u32_e32 v6, v12, v17
	v_ashrrev_i32_e32 v6, 31, v6
	v_sub_u32_e32 v13, v13, v6
	ds_read_b128 v[14:17], v9 offset:16704
	s_waitcnt lgkmcnt(0)
	v_sub_u32_e32 v6, v12, v14
	v_ashrrev_i32_e32 v6, 31, v6
	v_sub_u32_e32 v13, v13, v6
	v_sub_u32_e32 v6, v12, v15
	v_ashrrev_i32_e32 v6, 31, v6
	v_sub_u32_e32 v13, v13, v6
	v_sub_u32_e32 v6, v12, v16
	v_ashrrev_i32_e32 v6, 31, v6
	v_sub_u32_e32 v13, v13, v6
	v_sub_u32_e32 v6, v12, v17
	v_ashrrev_i32_e32 v6, 31, v6
	v_sub_u32_e32 v13, v13, v6
	ds_read_b128 v[14:17], v9 offset:16720
	s_waitcnt lgkmcnt(0)
	v_sub_u32_e32 v6, v12, v14
	v_ashrrev_i32_e32 v6, 31, v6
	v_sub_u32_e32 v13, v13, v6
	v_sub_u32_e32 v6, v12, v15
	v_ashrrev_i32_e32 v6, 31, v6
	v_sub_u32_e32 v13, v13, v6
	v_sub_u32_e32 v6, v12, v16
	v_ashrrev_i32_e32 v6, 31, v6
	v_sub_u32_e32 v13, v13, v6
	v_sub_u32_e32 v6, v12, v17
	v_ashrrev_i32_e32 v6, 31, v6
	v_sub_u32_e32 v13, v13, v6
	v_lshl_add_u32 v6, v13, 2, v9
	v_cmp_gt_u32_e32 vcc, 32, v5
	s_and_saveexec_b64 s[10:11], vcc
	ds_write_b32 v6, v5 offset:16768
	s_mov_b64 exec, s[10:11]
	v_bfe_u32 v6, v0, 4, 5
	v_lshl_add_u32 v6, v6, 2, v9
	ds_read_b32 v7, v6 offset:16768
	s_waitcnt lgkmcnt(0)
	v_add_u32_e32 v98, s2, v7
	v_lshl_add_u32 v7, v7, 2, v9
	ds_read_b32 v4, v7 offset:16448
	ds_read_b32 v6, v7 offset:16452
	v_ashrrev_i32_e32 v99, 31, v98
	v_mov_b32_e32 v2, 0
	s_waitcnt lgkmcnt(0)
	v_sub_u32_e32 v101, v6, v4
	v_cmp_gt_i32_e64 s[2:3], s4, v98
	s_mov_b64 s[4:5], exec
	s_nop 1
	v_cndmask_b32_e64 v4, 0, v4, s[2:3]
	v_cndmask_b32_e64 v101, 0, v101, s[2:3]

.LBB4_10:
	s_or_b64 exec, exec, s[4:5]
	s_waitcnt vmcnt(0)
	v_ashrrev_i32_e32 v12, 5, v2
	v_ashrrev_i32_e32 v13, 31, v12
	v_ashrrev_i32_e32 v14, 5, v6
	v_ashrrev_i32_e32 v16, 5, v4
	v_ashrrev_i32_e32 v18, 5, v8
	s_waitcnt lgkmcnt(0)
	v_lshl_add_u64 v[12:13], v[12:13], 2, s[16:17]
	v_ashrrev_i32_e32 v15, 31, v14
	v_ashrrev_i32_e32 v17, 31, v16
	v_ashrrev_i32_e32 v19, 31, v18
	v_lshl_add_u64 v[14:15], v[14:15], 2, s[16:17]
	v_lshl_add_u64 v[16:17], v[16:17], 2, s[16:17]
	v_lshl_add_u64 v[18:19], v[18:19], 2, s[16:17]
	global_load_dword v20, v[12:13], off
	global_load_dword v21, v[14:15], off
	global_load_dword v22, v[16:17], off
	global_load_dword v23, v[18:19], off
	s_load_dwordx2 s[14:15], s[0:1], 0x58
	s_load_dwordx4 s[8:11], s[0:1], 0x28
	v_max_i32_e32 v103, v10, v11
	v_lshlrev_b32_e32 v10, 5, v0
	v_and_b32_e32 v121, 0x3e00, v10
	v_lshlrev_b32_e32 v100, 4, v116
	v_mov_b32_e32 v108, 0
	v_mov_b32_e32 v115, 0
	v_mov_b32_e32 v114, 0
	v_mov_b32_e32 v113, 0
	v_mov_b32_e32 v112, 0
	v_mov_b32_e32 v111, 0
	v_cmp_lt_i32_e32 vcc, 0, v103
	v_lshl_or_b32 v122, v116, 3, v121
	v_mov_b32_e32 v110, 0
	s_waitcnt vmcnt(3)
	v_mul_f32_e32 v3, v3, v20
	s_waitcnt vmcnt(2)
	v_mul_f32_e32 v7, v7, v21
	s_waitcnt vmcnt(1)
	v_mul_f32_e32 v5, v5, v22
	s_waitcnt vmcnt(0)
	v_mul_f32_e32 v9, v9, v23
	ds_write2_b64 v122, v[2:3], v[6:7] offset1:16
	ds_write2_b64 v122, v[4:5], v[8:9] offset0:32 offset1:48
	s_and_saveexec_b64 s[18:19], vcc
	s_cbranch_execz .LBB4_28
	ds_read_b128 v[22:25], v121
	ds_read_b128 v[14:17], v121 offset:16
	s_mov_b64 s[20:21], s[40:41]
	v_cmp_lt_i32_e32 vcc, 16, v103
	s_waitcnt lgkmcnt(0)
	v_lshl_or_b32 v2, v22, 8, v100
	global_load_dwordx4 v[52:55], v2, s[20:21]
	v_lshl_or_b32 v2, v24, 8, v100
	global_load_dwordx4 v[48:51], v2, s[20:21]
	v_lshl_or_b32 v2, v14, 8, v100
	global_load_dwordx4 v[44:47], v2, s[20:21]
	v_lshl_or_b32 v2, v16, 8, v100
	global_load_dwordx4 v[36:39], v2, s[20:21]
	ds_read_b128 v[18:21], v121 offset:32
	ds_read_b128 v[2:5], v121 offset:48
	v_mov_b32_e32 v16, v25
	s_waitcnt lgkmcnt(1)
	v_lshl_or_b32 v6, v18, 8, v100
	global_load_dwordx4 v[32:35], v6, s[20:21]
	v_lshl_or_b32 v6, v20, 8, v100
	global_load_dwordx4 v[64:67], v6, s[20:21]
	s_waitcnt lgkmcnt(0)
	v_lshl_or_b32 v24, v2, 8, v100
	ds_read_b128 v[10:13], v121 offset:64
	ds_read_b128 v[6:9], v121 offset:80
	global_load_dwordx4 v[60:63], v24, s[20:21]
	v_lshl_or_b32 v25, v4, 8, v100
	v_mov_b32_e32 v20, v17
	s_waitcnt lgkmcnt(1)
	v_lshl_or_b32 v17, v10, 8, v100
	s_waitcnt lgkmcnt(0)
	v_lshl_or_b32 v24, v6, 8, v100
	v_lshl_or_b32 v12, v12, 8, v100
	global_load_dwordx4 v[56:59], v25, s[20:21]
	global_load_dwordx4 v[40:43], v17, s[20:21]
	global_load_dwordx4 v[28:31], v12, s[20:21]
	s_nop 0
	global_load_dwordx4 v[24:27], v24, s[20:21]
	v_mov_b32_e32 v4, v21
	v_lshl_or_b32 v8, v8, 8, v100
	s_waitcnt vmcnt(10)
	v_cvt_f32_f16_e32 v68, v52
	v_cvt_f32_f16_sdwa v69, v52 dst_sel:DWORD dst_unused:UNUSED_PAD src0_sel:WORD_1
	v_cvt_f32_f16_e32 v52, v53
	v_cvt_f32_f16_sdwa v53, v53 dst_sel:DWORD dst_unused:UNUSED_PAD src0_sel:WORD_1
	v_cvt_f32_f16_e32 v70, v54
	v_cvt_f32_f16_sdwa v71, v54 dst_sel:DWORD dst_unused:UNUSED_PAD src0_sel:WORD_1
	v_cvt_f32_f16_e32 v54, v55
	v_cvt_f32_f16_sdwa v55, v55 dst_sel:DWORD dst_unused:UNUSED_PAD src0_sel:WORD_1
	s_waitcnt vmcnt(9)
	v_cvt_f32_f16_e32 v72, v48
	v_cvt_f32_f16_sdwa v73, v48 dst_sel:DWORD dst_unused:UNUSED_PAD src0_sel:WORD_1
	v_cvt_f32_f16_e32 v48, v49
	v_cvt_f32_f16_sdwa v49, v49 dst_sel:DWORD dst_unused:UNUSED_PAD src0_sel:WORD_1
	v_cvt_f32_f16_e32 v74, v50
	v_cvt_f32_f16_sdwa v75, v50 dst_sel:DWORD dst_unused:UNUSED_PAD src0_sel:WORD_1
	v_cvt_f32_f16_e32 v50, v51
	v_cvt_f32_f16_sdwa v51, v51 dst_sel:DWORD dst_unused:UNUSED_PAD src0_sel:WORD_1
	s_waitcnt vmcnt(8)
	v_cvt_f32_f16_e32 v76, v44
	v_cvt_f32_f16_sdwa v77, v44 dst_sel:DWORD dst_unused:UNUSED_PAD src0_sel:WORD_1
	v_cvt_f32_f16_e32 v44, v45
	v_cvt_f32_f16_sdwa v45, v45 dst_sel:DWORD dst_unused:UNUSED_PAD src0_sel:WORD_1
	v_cvt_f32_f16_e32 v78, v46
	v_cvt_f32_f16_sdwa v79, v46 dst_sel:DWORD dst_unused:UNUSED_PAD src0_sel:WORD_1
	v_cvt_f32_f16_e32 v46, v47
	v_cvt_f32_f16_sdwa v47, v47 dst_sel:DWORD dst_unused:UNUSED_PAD src0_sel:WORD_1
	s_waitcnt vmcnt(7)
	v_cvt_f32_f16_e32 v80, v36
	v_cvt_f32_f16_sdwa v81, v36 dst_sel:DWORD dst_unused:UNUSED_PAD src0_sel:WORD_1
	v_cvt_f32_f16_e32 v36, v37
	v_cvt_f32_f16_sdwa v37, v37 dst_sel:DWORD dst_unused:UNUSED_PAD src0_sel:WORD_1
	v_cvt_f32_f16_e32 v82, v38
	v_cvt_f32_f16_sdwa v83, v38 dst_sel:DWORD dst_unused:UNUSED_PAD src0_sel:WORD_1
	v_cvt_f32_f16_e32 v38, v39
	v_cvt_f32_f16_sdwa v39, v39 dst_sel:DWORD dst_unused:UNUSED_PAD src0_sel:WORD_1
	s_waitcnt vmcnt(6)
	v_cvt_f32_f16_e32 v84, v32
	v_cvt_f32_f16_sdwa v85, v32 dst_sel:DWORD dst_unused:UNUSED_PAD src0_sel:WORD_1
	v_cvt_f32_f16_e32 v32, v33
	v_cvt_f32_f16_sdwa v33, v33 dst_sel:DWORD dst_unused:UNUSED_PAD src0_sel:WORD_1
	v_pk_fma_f32 v[68:69], v[68:69], v[22:23], 0 op_sel:[0,1,0] op_sel_hi:[1,1,0]
	v_pk_fma_f32 v[52:53], v[52:53], v[22:23], 0 op_sel:[0,1,0] op_sel_hi:[1,1,0]
	v_cvt_f32_f16_e32 v86, v34
	v_cvt_f32_f16_sdwa v87, v34 dst_sel:DWORD dst_unused:UNUSED_PAD src0_sel:WORD_1
	v_cvt_f32_f16_e32 v34, v35
	v_cvt_f32_f16_sdwa v35, v35 dst_sel:DWORD dst_unused:UNUSED_PAD src0_sel:WORD_1
	s_waitcnt vmcnt(5)
	v_cvt_f32_f16_e32 v88, v64
	v_cvt_f32_f16_sdwa v89, v64 dst_sel:DWORD dst_unused:UNUSED_PAD src0_sel:WORD_1
	v_cvt_f32_f16_e32 v64, v65
	v_pk_fma_f32 v[70:71], v[70:71], v[22:23], 0 op_sel:[0,1,0] op_sel_hi:[1,1,0]
	v_pk_fma_f32 v[22:23], v[54:55], v[22:23], 0 op_sel:[0,1,0] op_sel_hi:[1,1,0]
	v_pk_fma_f32 v[54:55], v[72:73], v[16:17], v[68:69] op_sel_hi:[1,0,1]
	v_pk_fma_f32 v[48:49], v[48:49], v[16:17], v[52:53] op_sel_hi:[1,0,1]
	v_cvt_f32_f16_sdwa v65, v65 dst_sel:DWORD dst_unused:UNUSED_PAD src0_sel:WORD_1
	v_pk_fma_f32 v[52:53], v[74:75], v[16:17], v[70:71] op_sel_hi:[1,0,1]
	v_pk_fma_f32 v[16:17], v[50:51], v[16:17], v[22:23] op_sel_hi:[1,0,1]
	v_pk_fma_f32 v[22:23], v[76:77], v[14:15], v[54:55] op_sel:[0,1,0]
	v_pk_fma_f32 v[44:45], v[44:45], v[14:15], v[48:49] op_sel:[0,1,0]
	v_pk_fma_f32 v[48:49], v[78:79], v[14:15], v[52:53] op_sel:[0,1,0]
	v_pk_fma_f32 v[14:15], v[46:47], v[14:15], v[16:17] op_sel:[0,1,0]
	v_pk_fma_f32 v[16:17], v[80:81], v[20:21], v[22:23] op_sel_hi:[1,0,1]
	v_pk_fma_f32 v[22:23], v[36:37], v[20:21], v[44:45] op_sel_hi:[1,0,1]
	v_pk_fma_f32 v[36:37], v[82:83], v[20:21], v[48:49] op_sel_hi:[1,0,1]
	v_pk_fma_f32 v[14:15], v[38:39], v[20:21], v[14:15] op_sel_hi:[1,0,1]
	v_pk_fma_f32 v[20:21], v[32:33], v[18:19], v[22:23] op_sel:[0,1,0]
	v_cvt_f32_f16_e32 v46, v66
	v_cvt_f32_f16_sdwa v47, v66 dst_sel:DWORD dst_unused:UNUSED_PAD src0_sel:WORD_1
	v_cvt_f32_f16_e32 v52, v67
	v_cvt_f32_f16_sdwa v53, v67 dst_sel:DWORD dst_unused:UNUSED_PAD src0_sel:WORD_1
	s_waitcnt vmcnt(4)
	v_cvt_f32_f16_e32 v54, v60
	v_cvt_f32_f16_sdwa v55, v60 dst_sel:DWORD dst_unused:UNUSED_PAD src0_sel:WORD_1
	v_cvt_f32_f16_e32 v60, v61
	v_cvt_f32_f16_sdwa v61, v61 dst_sel:DWORD dst_unused:UNUSED_PAD src0_sel:WORD_1
	v_pk_fma_f32 v[16:17], v[84:85], v[18:19], v[16:17] op_sel:[0,1,0]
	v_pk_fma_f32 v[22:23], v[86:87], v[18:19], v[36:37] op_sel:[0,1,0]
	v_pk_fma_f32 v[44:45], v[34:35], v[18:19], v[14:15] op_sel:[0,1,0]
	v_pk_fma_f32 v[50:51], v[64:65], v[4:5], v[20:21] op_sel_hi:[1,0,1]
	ds_read_b128 v[18:21], v121 offset:96
	v_pk_fma_f32 v[48:49], v[88:89], v[4:5], v[16:17] op_sel_hi:[1,0,1]
	ds_read_b128 v[14:17], v121 offset:112
	v_pk_fma_f32 v[22:23], v[46:47], v[4:5], v[22:23] op_sel_hi:[1,0,1]
	v_pk_fma_f32 v[44:45], v[52:53], v[4:5], v[44:45] op_sel_hi:[1,0,1]
	v_pk_fma_f32 v[46:47], v[54:55], v[2:3], v[48:49] op_sel:[0,1,0]
	v_pk_fma_f32 v[52:53], v[60:61], v[2:3], v[50:51] op_sel:[0,1,0]
	v_cvt_f32_f16_e32 v54, v62
	v_cvt_f32_f16_sdwa v55, v62 dst_sel:DWORD dst_unused:UNUSED_PAD src0_sel:WORD_1
	v_cvt_f32_f16_e32 v60, v63
	v_cvt_f32_f16_sdwa v61, v63 dst_sel:DWORD dst_unused:UNUSED_PAD src0_sel:WORD_1
	s_waitcnt vmcnt(3)
	v_cvt_f32_f16_e32 v62, v56
	v_cvt_f32_f16_sdwa v63, v56 dst_sel:DWORD dst_unused:UNUSED_PAD src0_sel:WORD_1
	v_cvt_f32_f16_e32 v56, v57
	v_cvt_f32_f16_sdwa v57, v57 dst_sel:DWORD dst_unused:UNUSED_PAD src0_sel:WORD_1
	v_cvt_f32_f16_e32 v64, v58
	v_cvt_f32_f16_sdwa v65, v58 dst_sel:DWORD dst_unused:UNUSED_PAD src0_sel:WORD_1
	v_cvt_f32_f16_e32 v58, v59
	v_cvt_f32_f16_sdwa v59, v59 dst_sel:DWORD dst_unused:UNUSED_PAD src0_sel:WORD_1
	s_waitcnt lgkmcnt(1)
	v_lshl_or_b32 v4, v20, 8, v100
	global_load_dwordx4 v[32:35], v8, s[20:21]
	global_load_dwordx4 v[48:51], v4, s[20:21]
	v_mov_b32_e32 v4, v5
	v_pk_fma_f32 v[22:23], v[54:55], v[2:3], v[22:23] op_sel:[0,1,0]
	v_pk_fma_f32 v[2:3], v[60:61], v[2:3], v[44:45] op_sel:[0,1,0]
	v_pk_fma_f32 v[54:55], v[62:63], v[4:5], v[46:47] op_sel_hi:[1,0,1]
	v_pk_fma_f32 v[52:53], v[56:57], v[4:5], v[52:53] op_sel_hi:[1,0,1]
	s_waitcnt lgkmcnt(0)
	v_lshl_or_b32 v5, v14, 8, v100
	v_pk_fma_f32 v[56:57], v[58:59], v[4:5], v[2:3] op_sel_hi:[1,0,1]
	v_lshl_or_b32 v2, v16, 8, v100
	global_load_dwordx4 v[44:47], v5, s[20:21]
	v_pk_fma_f32 v[22:23], v[64:65], v[4:5], v[22:23] op_sel_hi:[1,0,1]
	global_load_dwordx4 v[2:5], v2, s[20:21]
	v_lshl_or_b32 v8, v18, 8, v100
	global_load_dwordx4 v[36:39], v8, s[20:21]
	s_waitcnt vmcnt(7)
	v_cvt_f32_f16_e32 v58, v40
	v_cvt_f32_f16_sdwa v59, v40 dst_sel:DWORD dst_unused:UNUSED_PAD src0_sel:WORD_1
	v_cvt_f32_f16_e32 v40, v41
	v_cvt_f32_f16_sdwa v41, v41 dst_sel:DWORD dst_unused:UNUSED_PAD src0_sel:WORD_1
	v_cvt_f32_f16_e32 v60, v42
	v_cvt_f32_f16_sdwa v61, v42 dst_sel:DWORD dst_unused:UNUSED_PAD src0_sel:WORD_1
	v_cvt_f32_f16_e32 v42, v43
	v_cvt_f32_f16_sdwa v43, v43 dst_sel:DWORD dst_unused:UNUSED_PAD src0_sel:WORD_1
	s_waitcnt vmcnt(6)
	v_cvt_f32_f16_e32 v62, v28
	v_cvt_f32_f16_sdwa v63, v28 dst_sel:DWORD dst_unused:UNUSED_PAD src0_sel:WORD_1
	v_cvt_f32_f16_e32 v28, v29
	v_cvt_f32_f16_sdwa v29, v29 dst_sel:DWORD dst_unused:UNUSED_PAD src0_sel:WORD_1
	v_cvt_f32_f16_e32 v64, v30
	v_cvt_f32_f16_sdwa v65, v30 dst_sel:DWORD dst_unused:UNUSED_PAD src0_sel:WORD_1
	v_cvt_f32_f16_e32 v30, v31
	v_cvt_f32_f16_sdwa v31, v31 dst_sel:DWORD dst_unused:UNUSED_PAD src0_sel:WORD_1
	v_pk_fma_f32 v[54:55], v[58:59], v[10:11], v[54:55] op_sel:[0,1,0]
	v_pk_fma_f32 v[40:41], v[40:41], v[10:11], v[52:53] op_sel:[0,1,0]
	v_pk_fma_f32 v[22:23], v[60:61], v[10:11], v[22:23] op_sel:[0,1,0]
	v_pk_fma_f32 v[10:11], v[42:43], v[10:11], v[56:57] op_sel:[0,1,0]
	v_mov_b32_e32 v8, v13
	v_pk_fma_f32 v[28:29], v[28:29], v[8:9], v[40:41] op_sel_hi:[1,0,1]
	v_pk_fma_f32 v[10:11], v[30:31], v[8:9], v[10:11] op_sel_hi:[1,0,1]
	s_waitcnt vmcnt(5)
	v_cvt_f32_f16_e32 v30, v24
	v_cvt_f32_f16_sdwa v31, v24 dst_sel:DWORD dst_unused:UNUSED_PAD src0_sel:WORD_1
	v_cvt_f32_f16_e32 v24, v25
	v_cvt_f32_f16_sdwa v25, v25 dst_sel:DWORD dst_unused:UNUSED_PAD src0_sel:WORD_1
	v_cvt_f32_f16_e32 v40, v26
	v_cvt_f32_f16_sdwa v41, v26 dst_sel:DWORD dst_unused:UNUSED_PAD src0_sel:WORD_1
	v_cvt_f32_f16_e32 v26, v27
	v_cvt_f32_f16_sdwa v27, v27 dst_sel:DWORD dst_unused:UNUSED_PAD src0_sel:WORD_1
	v_pk_fma_f32 v[12:13], v[62:63], v[8:9], v[54:55] op_sel_hi:[1,0,1]
	v_pk_fma_f32 v[22:23], v[64:65], v[8:9], v[22:23] op_sel_hi:[1,0,1]
	v_pk_fma_f32 v[12:13], v[30:31], v[6:7], v[12:13] op_sel:[0,1,0]
	v_pk_fma_f32 v[24:25], v[24:25], v[6:7], v[28:29] op_sel:[0,1,0]
	v_pk_fma_f32 v[22:23], v[40:41], v[6:7], v[22:23] op_sel:[0,1,0]
	v_pk_fma_f32 v[6:7], v[26:27], v[6:7], v[10:11] op_sel:[0,1,0]
	v_mov_b32_e32 v8, v9
	v_mov_b32_e32 v16, v21
	s_waitcnt vmcnt(4)
	v_cvt_f32_f16_e32 v10, v32
	v_cvt_f32_f16_sdwa v11, v32 dst_sel:DWORD dst_unused:UNUSED_PAD src0_sel:WORD_1
	v_cvt_f32_f16_e32 v26, v33
	v_cvt_f32_f16_sdwa v27, v33 dst_sel:DWORD dst_unused:UNUSED_PAD src0_sel:WORD_1
	v_cvt_f32_f16_e32 v28, v34
	v_cvt_f32_f16_sdwa v29, v34 dst_sel:DWORD dst_unused:UNUSED_PAD src0_sel:WORD_1
	v_cvt_f32_f16_e32 v30, v35
	v_cvt_f32_f16_sdwa v31, v35 dst_sel:DWORD dst_unused:UNUSED_PAD src0_sel:WORD_1
	v_pk_fma_f32 v[10:11], v[10:11], v[8:9], v[12:13] op_sel_hi:[1,0,1]
	v_pk_fma_f32 v[12:13], v[26:27], v[8:9], v[24:25] op_sel_hi:[1,0,1]
	v_pk_fma_f32 v[22:23], v[28:29], v[8:9], v[22:23] op_sel_hi:[1,0,1]
	v_pk_fma_f32 v[6:7], v[30:31], v[8:9], v[6:7] op_sel_hi:[1,0,1]
	s_waitcnt vmcnt(3)
	v_cvt_f32_f16_e32 v20, v49
	v_cvt_f32_f16_sdwa v21, v49 dst_sel:DWORD dst_unused:UNUSED_PAD src0_sel:WORD_1
	s_waitcnt vmcnt(0)
	v_cvt_f32_f16_e32 v8, v36
	v_cvt_f32_f16_sdwa v9, v36 dst_sel:DWORD dst_unused:UNUSED_PAD src0_sel:WORD_1
	v_cvt_f32_f16_e32 v24, v37
	v_cvt_f32_f16_sdwa v25, v37 dst_sel:DWORD dst_unused:UNUSED_PAD src0_sel:WORD_1
	v_cvt_f32_f16_e32 v26, v38
	v_cvt_f32_f16_sdwa v27, v38 dst_sel:DWORD dst_unused:UNUSED_PAD src0_sel:WORD_1
	v_cvt_f32_f16_e32 v28, v39
	v_cvt_f32_f16_sdwa v29, v39 dst_sel:DWORD dst_unused:UNUSED_PAD src0_sel:WORD_1
	v_pk_fma_f32 v[8:9], v[8:9], v[18:19], v[10:11] op_sel:[0,1,0]
	v_pk_fma_f32 v[10:11], v[24:25], v[18:19], v[12:13] op_sel:[0,1,0]
	v_pk_fma_f32 v[12:13], v[26:27], v[18:19], v[22:23] op_sel:[0,1,0]
	v_pk_fma_f32 v[6:7], v[28:29], v[18:19], v[6:7] op_sel:[0,1,0]
	v_cvt_f32_f16_e32 v18, v48
	v_cvt_f32_f16_sdwa v19, v48 dst_sel:DWORD dst_unused:UNUSED_PAD src0_sel:WORD_1
	v_cvt_f32_f16_e32 v22, v50
	v_cvt_f32_f16_sdwa v23, v50 dst_sel:DWORD dst_unused:UNUSED_PAD src0_sel:WORD_1
	v_cvt_f32_f16_e32 v24, v51
	v_cvt_f32_f16_sdwa v25, v51 dst_sel:DWORD dst_unused:UNUSED_PAD src0_sel:WORD_1
	v_pk_fma_f32 v[8:9], v[18:19], v[16:17], v[8:9] op_sel_hi:[1,0,1]
	v_pk_fma_f32 v[10:11], v[20:21], v[16:17], v[10:11] op_sel_hi:[1,0,1]
	v_pk_fma_f32 v[12:13], v[22:23], v[16:17], v[12:13] op_sel_hi:[1,0,1]
	v_pk_fma_f32 v[6:7], v[24:25], v[16:17], v[6:7] op_sel_hi:[1,0,1]
	v_cvt_f32_f16_e32 v18, v44
	v_cvt_f32_f16_sdwa v19, v44 dst_sel:DWORD dst_unused:UNUSED_PAD src0_sel:WORD_1
	v_cvt_f32_f16_e32 v20, v45
	v_cvt_f32_f16_sdwa v21, v45 dst_sel:DWORD dst_unused:UNUSED_PAD src0_sel:WORD_1
	v_cvt_f32_f16_e32 v22, v46
	v_cvt_f32_f16_sdwa v23, v46 dst_sel:DWORD dst_unused:UNUSED_PAD src0_sel:WORD_1
	v_cvt_f32_f16_e32 v24, v47
	v_cvt_f32_f16_sdwa v25, v47 dst_sel:DWORD dst_unused:UNUSED_PAD src0_sel:WORD_1
	v_pk_fma_f32 v[8:9], v[18:19], v[14:15], v[8:9] op_sel:[0,1,0]
	v_pk_fma_f32 v[10:11], v[20:21], v[14:15], v[10:11] op_sel:[0,1,0]
	v_pk_fma_f32 v[12:13], v[22:23], v[14:15], v[12:13] op_sel:[0,1,0]
	v_pk_fma_f32 v[6:7], v[24:25], v[14:15], v[6:7] op_sel:[0,1,0]
	v_mov_b32_e32 v14, v17
	v_cvt_f32_f16_e32 v16, v2
	v_cvt_f32_f16_sdwa v17, v2 dst_sel:DWORD dst_unused:UNUSED_PAD src0_sel:WORD_1
	v_cvt_f32_f16_e32 v2, v3
	v_cvt_f32_f16_sdwa v3, v3 dst_sel:DWORD dst_unused:UNUSED_PAD src0_sel:WORD_1
	v_cvt_f32_f16_e32 v18, v4
	v_cvt_f32_f16_sdwa v19, v4 dst_sel:DWORD dst_unused:UNUSED_PAD src0_sel:WORD_1
	v_cvt_f32_f16_e32 v4, v5
	v_cvt_f32_f16_sdwa v5, v5 dst_sel:DWORD dst_unused:UNUSED_PAD src0_sel:WORD_1
	v_pk_fma_f32 v[110:111], v[16:17], v[14:15], v[8:9] op_sel_hi:[1,0,1]
	v_pk_fma_f32 v[112:113], v[2:3], v[14:15], v[10:11] op_sel_hi:[1,0,1]
	v_pk_fma_f32 v[114:115], v[18:19], v[14:15], v[12:13] op_sel_hi:[1,0,1]
	v_pk_fma_f32 v[108:109], v[4:5], v[14:15], v[6:7] op_sel_hi:[1,0,1]
	s_and_saveexec_b64 s[4:5], vcc
	s_cbranch_execz .LBB4_13
	ds_read_b128 v[30:33], v121 offset:128
	ds_read_b128 v[22:25], v121 offset:144
	s_waitcnt lgkmcnt(1)
	v_lshl_or_b32 v2, v30, 8, v100
	global_load_dwordx4 v[60:63], v2, s[20:21]
	v_lshl_or_b32 v2, v32, 8, v100
	global_load_dwordx4 v[52:55], v2, s[20:21]
	s_waitcnt lgkmcnt(0)
	v_lshl_or_b32 v2, v22, 8, v100
	global_load_dwordx4 v[44:47], v2, s[20:21]
	v_lshl_or_b32 v2, v24, 8, v100
	global_load_dwordx4 v[40:43], v2, s[20:21]
	ds_read_b128 v[14:17], v121 offset:160
	ds_read_b128 v[6:9], v121 offset:176
	s_waitcnt lgkmcnt(1)
	v_lshl_or_b32 v2, v14, 8, v100
	global_load_dwordx4 v[36:39], v2, s[20:21]
	v_lshl_or_b32 v2, v16, 8, v100
	global_load_dwordx4 v[18:21], v2, s[20:21]
	ds_read_b128 v[56:59], v121 offset:192
	ds_read_b128 v[26:29], v121 offset:208
	ds_read_b128 v[10:13], v121 offset:224
	ds_read_b128 v[2:5], v121 offset:240
	s_waitcnt lgkmcnt(4)
	v_lshl_or_b32 v24, v6, 8, v100
	v_lshl_or_b32 v32, v8, 8, v100
	v_mov_b32_e32 v8, v33
	s_waitcnt lgkmcnt(3)
	v_lshl_or_b32 v33, v56, 8, v100
	v_lshl_or_b32 v34, v58, 8, v100
	s_waitcnt lgkmcnt(2)
	v_lshl_or_b32 v35, v26, 8, v100
	v_mov_b32_e32 v16, v25
	v_lshl_or_b32 v25, v28, 8, v100
	global_load_dwordx4 v[76:79], v24, s[20:21]
	global_load_dwordx4 v[72:75], v32, s[20:21]
	global_load_dwordx4 v[68:71], v33, s[20:21]
	global_load_dwordx4 v[64:67], v34, s[20:21]
	global_load_dwordx4 v[48:51], v35, s[20:21]
	s_nop 0
	global_load_dwordx4 v[32:35], v25, s[20:21]
	s_waitcnt lgkmcnt(1)
	v_lshl_or_b32 v28, v10, 8, v100
	v_lshl_or_b32 v12, v12, 8, v100
	s_waitcnt lgkmcnt(0)
	v_lshl_or_b32 v4, v4, 8, v100
	s_waitcnt vmcnt(11)
	v_cvt_f32_f16_e32 v24, v60
	v_cvt_f32_f16_sdwa v25, v60 dst_sel:DWORD dst_unused:UNUSED_PAD src0_sel:WORD_1
	v_cvt_f32_f16_e32 v60, v61
	v_cvt_f32_f16_sdwa v61, v61 dst_sel:DWORD dst_unused:UNUSED_PAD src0_sel:WORD_1
	v_cvt_f32_f16_e32 v80, v62
	v_cvt_f32_f16_sdwa v81, v62 dst_sel:DWORD dst_unused:UNUSED_PAD src0_sel:WORD_1
	v_cvt_f32_f16_e32 v62, v63
	v_cvt_f32_f16_sdwa v63, v63 dst_sel:DWORD dst_unused:UNUSED_PAD src0_sel:WORD_1
	s_waitcnt vmcnt(10)
	v_cvt_f32_f16_e32 v82, v52
	v_cvt_f32_f16_sdwa v83, v52 dst_sel:DWORD dst_unused:UNUSED_PAD src0_sel:WORD_1
	v_cvt_f32_f16_e32 v52, v53
	v_cvt_f32_f16_sdwa v53, v53 dst_sel:DWORD dst_unused:UNUSED_PAD src0_sel:WORD_1
	v_cvt_f32_f16_e32 v84, v54
	v_cvt_f32_f16_sdwa v85, v54 dst_sel:DWORD dst_unused:UNUSED_PAD src0_sel:WORD_1
	v_cvt_f32_f16_e32 v54, v55
	v_cvt_f32_f16_sdwa v55, v55 dst_sel:DWORD dst_unused:UNUSED_PAD src0_sel:WORD_1
	s_waitcnt vmcnt(9)
	v_cvt_f32_f16_e32 v86, v44
	v_cvt_f32_f16_sdwa v87, v44 dst_sel:DWORD dst_unused:UNUSED_PAD src0_sel:WORD_1
	v_cvt_f32_f16_e32 v44, v45
	v_cvt_f32_f16_sdwa v45, v45 dst_sel:DWORD dst_unused:UNUSED_PAD src0_sel:WORD_1
	v_cvt_f32_f16_e32 v88, v46
	v_cvt_f32_f16_sdwa v89, v46 dst_sel:DWORD dst_unused:UNUSED_PAD src0_sel:WORD_1
	v_cvt_f32_f16_e32 v46, v47
	v_cvt_f32_f16_sdwa v47, v47 dst_sel:DWORD dst_unused:UNUSED_PAD src0_sel:WORD_1
	s_waitcnt vmcnt(8)
	v_cvt_f32_f16_e32 v90, v40
	v_cvt_f32_f16_sdwa v91, v40 dst_sel:DWORD dst_unused:UNUSED_PAD src0_sel:WORD_1
	v_cvt_f32_f16_e32 v40, v41
	v_cvt_f32_f16_sdwa v41, v41 dst_sel:DWORD dst_unused:UNUSED_PAD src0_sel:WORD_1
	v_cvt_f32_f16_e32 v92, v42
	v_cvt_f32_f16_sdwa v93, v42 dst_sel:DWORD dst_unused:UNUSED_PAD src0_sel:WORD_1
	v_cvt_f32_f16_e32 v42, v43
	v_cvt_f32_f16_sdwa v43, v43 dst_sel:DWORD dst_unused:UNUSED_PAD src0_sel:WORD_1
	s_waitcnt vmcnt(7)
	v_cvt_f32_f16_e32 v94, v36
	v_cvt_f32_f16_sdwa v95, v36 dst_sel:DWORD dst_unused:UNUSED_PAD src0_sel:WORD_1
	v_cvt_f32_f16_e32 v36, v37
	v_cvt_f32_f16_sdwa v37, v37 dst_sel:DWORD dst_unused:UNUSED_PAD src0_sel:WORD_1
	v_cvt_f32_f16_e32 v96, v38
	v_cvt_f32_f16_sdwa v97, v38 dst_sel:DWORD dst_unused:UNUSED_PAD src0_sel:WORD_1
	v_cvt_f32_f16_e32 v38, v39
	v_cvt_f32_f16_sdwa v39, v39 dst_sel:DWORD dst_unused:UNUSED_PAD src0_sel:WORD_1
	v_pk_fma_f32 v[24:25], v[24:25], v[30:31], v[110:111] op_sel:[0,1,0]
	v_pk_fma_f32 v[60:61], v[60:61], v[30:31], v[112:113] op_sel:[0,1,0]
	v_pk_fma_f32 v[80:81], v[80:81], v[30:31], v[114:115] op_sel:[0,1,0]
	v_pk_fma_f32 v[30:31], v[62:63], v[30:31], v[108:109] op_sel:[0,1,0]
	v_pk_fma_f32 v[24:25], v[82:83], v[8:9], v[24:25] op_sel_hi:[1,0,1]
	v_pk_fma_f32 v[52:53], v[52:53], v[8:9], v[60:61] op_sel_hi:[1,0,1]
	v_pk_fma_f32 v[60:61], v[84:85], v[8:9], v[80:81] op_sel_hi:[1,0,1]
	v_pk_fma_f32 v[30:31], v[54:55], v[8:9], v[30:31] op_sel_hi:[1,0,1]
	v_pk_fma_f32 v[24:25], v[86:87], v[22:23], v[24:25] op_sel:[0,1,0]
	v_pk_fma_f32 v[44:45], v[44:45], v[22:23], v[52:53] op_sel:[0,1,0]
	v_pk_fma_f32 v[52:53], v[88:89], v[22:23], v[60:61] op_sel:[0,1,0]
	v_pk_fma_f32 v[22:23], v[46:47], v[22:23], v[30:31] op_sel:[0,1,0]
	v_pk_fma_f32 v[24:25], v[90:91], v[16:17], v[24:25] op_sel_hi:[1,0,1]
	v_pk_fma_f32 v[30:31], v[40:41], v[16:17], v[44:45] op_sel_hi:[1,0,1]
	v_pk_fma_f32 v[40:41], v[92:93], v[16:17], v[52:53] op_sel_hi:[1,0,1]
	v_pk_fma_f32 v[22:23], v[42:43], v[16:17], v[22:23] op_sel_hi:[1,0,1]
	v_pk_fma_f32 v[24:25], v[94:95], v[14:15], v[24:25] op_sel:[0,1,0]
	v_pk_fma_f32 v[30:31], v[36:37], v[14:15], v[30:31] op_sel:[0,1,0]
	v_pk_fma_f32 v[40:41], v[96:97], v[14:15], v[40:41] op_sel:[0,1,0]
	v_pk_fma_f32 v[14:15], v[38:39], v[14:15], v[22:23] op_sel:[0,1,0]
	s_waitcnt vmcnt(6)
	v_cvt_f32_f16_e32 v22, v18
	v_cvt_f32_f16_sdwa v23, v18 dst_sel:DWORD dst_unused:UNUSED_PAD src0_sel:WORD_1
	v_cvt_f32_f16_e32 v42, v19
	v_cvt_f32_f16_sdwa v43, v19 dst_sel:DWORD dst_unused:UNUSED_PAD src0_sel:WORD_1
	v_cvt_f32_f16_e32 v44, v20
	v_cvt_f32_f16_sdwa v45, v20 dst_sel:DWORD dst_unused:UNUSED_PAD src0_sel:WORD_1
	v_cvt_f32_f16_e32 v46, v21
	v_cvt_f32_f16_sdwa v47, v21 dst_sel:DWORD dst_unused:UNUSED_PAD src0_sel:WORD_1
	global_load_dwordx4 v[36:39], v28, s[20:21]
	global_load_dwordx4 v[18:21], v12, s[20:21]
	v_lshl_or_b32 v12, v2, 8, v100
	v_mov_b32_e32 v8, v17
	v_pk_fma_f32 v[52:53], v[22:23], v[8:9], v[24:25] op_sel_hi:[1,0,1]
	v_pk_fma_f32 v[30:31], v[42:43], v[8:9], v[30:31] op_sel_hi:[1,0,1]
	v_pk_fma_f32 v[42:43], v[46:47], v[8:9], v[14:15] op_sel_hi:[1,0,1]
	global_load_dwordx4 v[22:25], v12, s[20:21]
	global_load_dwordx4 v[14:17], v4, s[20:21]
	v_pk_fma_f32 v[40:41], v[44:45], v[8:9], v[40:41] op_sel_hi:[1,0,1]
	s_waitcnt vmcnt(9)
	v_cvt_f32_f16_e32 v44, v76
	v_cvt_f32_f16_sdwa v45, v76 dst_sel:DWORD dst_unused:UNUSED_PAD src0_sel:WORD_1
	v_cvt_f32_f16_e32 v46, v77
	v_cvt_f32_f16_sdwa v47, v77 dst_sel:DWORD dst_unused:UNUSED_PAD src0_sel:WORD_1
	v_cvt_f32_f16_e32 v54, v78
	v_cvt_f32_f16_sdwa v55, v78 dst_sel:DWORD dst_unused:UNUSED_PAD src0_sel:WORD_1
	v_cvt_f32_f16_e32 v60, v79
	v_cvt_f32_f16_sdwa v61, v79 dst_sel:DWORD dst_unused:UNUSED_PAD src0_sel:WORD_1
	v_pk_fma_f32 v[44:45], v[44:45], v[6:7], v[52:53] op_sel:[0,1,0]
	v_pk_fma_f32 v[30:31], v[46:47], v[6:7], v[30:31] op_sel:[0,1,0]
	v_pk_fma_f32 v[40:41], v[54:55], v[6:7], v[40:41] op_sel:[0,1,0]
	v_pk_fma_f32 v[6:7], v[60:61], v[6:7], v[42:43] op_sel:[0,1,0]
	v_mov_b32_e32 v4, v9
	s_waitcnt vmcnt(8)
	v_cvt_f32_f16_e32 v8, v72
	v_cvt_f32_f16_sdwa v9, v72 dst_sel:DWORD dst_unused:UNUSED_PAD src0_sel:WORD_1
	v_cvt_f32_f16_e32 v42, v73
	v_cvt_f32_f16_sdwa v43, v73 dst_sel:DWORD dst_unused:UNUSED_PAD src0_sel:WORD_1
	v_cvt_f32_f16_e32 v46, v74
	v_cvt_f32_f16_sdwa v47, v74 dst_sel:DWORD dst_unused:UNUSED_PAD src0_sel:WORD_1
	v_cvt_f32_f16_e32 v52, v75
	v_cvt_f32_f16_sdwa v53, v75 dst_sel:DWORD dst_unused:UNUSED_PAD src0_sel:WORD_1
	v_pk_fma_f32 v[8:9], v[8:9], v[4:5], v[44:45] op_sel_hi:[1,0,1]
	v_pk_fma_f32 v[30:31], v[42:43], v[4:5], v[30:31] op_sel_hi:[1,0,1]
	v_pk_fma_f32 v[40:41], v[46:47], v[4:5], v[40:41] op_sel_hi:[1,0,1]
	s_waitcnt vmcnt(7)
	v_cvt_f32_f16_e32 v42, v68
	v_cvt_f32_f16_sdwa v43, v68 dst_sel:DWORD dst_unused:UNUSED_PAD src0_sel:WORD_1
	v_cvt_f32_f16_e32 v44, v69
	v_cvt_f32_f16_sdwa v45, v69 dst_sel:DWORD dst_unused:UNUSED_PAD src0_sel:WORD_1
	v_cvt_f32_f16_e32 v46, v70
	v_cvt_f32_f16_sdwa v47, v70 dst_sel:DWORD dst_unused:UNUSED_PAD src0_sel:WORD_1
	v_pk_fma_f32 v[6:7], v[52:53], v[4:5], v[6:7] op_sel_hi:[1,0,1]
	v_cvt_f32_f16_e32 v52, v71
	v_cvt_f32_f16_sdwa v53, v71 dst_sel:DWORD dst_unused:UNUSED_PAD src0_sel:WORD_1
	v_pk_fma_f32 v[8:9], v[42:43], v[56:57], v[8:9] op_sel:[0,1,0]
	v_pk_fma_f32 v[30:31], v[44:45], v[56:57], v[30:31] op_sel:[0,1,0]
	v_pk_fma_f32 v[40:41], v[46:47], v[56:57], v[40:41] op_sel:[0,1,0]
	s_waitcnt vmcnt(6)
	v_cvt_f32_f16_e32 v42, v64
	v_cvt_f32_f16_sdwa v43, v64 dst_sel:DWORD dst_unused:UNUSED_PAD src0_sel:WORD_1
	v_cvt_f32_f16_e32 v44, v65
	v_cvt_f32_f16_sdwa v45, v65 dst_sel:DWORD dst_unused:UNUSED_PAD src0_sel:WORD_1
	v_cvt_f32_f16_e32 v46, v66
	v_cvt_f32_f16_sdwa v47, v66 dst_sel:DWORD dst_unused:UNUSED_PAD src0_sel:WORD_1
	v_pk_fma_f32 v[6:7], v[52:53], v[56:57], v[6:7] op_sel:[0,1,0]
	v_mov_b32_e32 v4, v59
	v_cvt_f32_f16_e32 v52, v67
	v_cvt_f32_f16_sdwa v53, v67 dst_sel:DWORD dst_unused:UNUSED_PAD src0_sel:WORD_1
	v_pk_fma_f32 v[8:9], v[42:43], v[4:5], v[8:9] op_sel_hi:[1,0,1]
	v_pk_fma_f32 v[30:31], v[44:45], v[4:5], v[30:31] op_sel_hi:[1,0,1]
	v_pk_fma_f32 v[40:41], v[46:47], v[4:5], v[40:41] op_sel_hi:[1,0,1]
	s_waitcnt vmcnt(5)
	v_cvt_f32_f16_e32 v42, v48
	v_cvt_f32_f16_sdwa v43, v48 dst_sel:DWORD dst_unused:UNUSED_PAD src0_sel:WORD_1
	v_cvt_f32_f16_e32 v44, v49
	v_cvt_f32_f16_sdwa v45, v49 dst_sel:DWORD dst_unused:UNUSED_PAD src0_sel:WORD_1
	v_cvt_f32_f16_e32 v46, v50
	v_cvt_f32_f16_sdwa v47, v50 dst_sel:DWORD dst_unused:UNUSED_PAD src0_sel:WORD_1
	v_cvt_f32_f16_e32 v48, v51
	v_cvt_f32_f16_sdwa v49, v51 dst_sel:DWORD dst_unused:UNUSED_PAD src0_sel:WORD_1
	v_pk_fma_f32 v[6:7], v[52:53], v[4:5], v[6:7] op_sel_hi:[1,0,1]
	v_pk_fma_f32 v[8:9], v[42:43], v[26:27], v[8:9] op_sel:[0,1,0]
	v_pk_fma_f32 v[30:31], v[44:45], v[26:27], v[30:31] op_sel:[0,1,0]
	v_pk_fma_f32 v[40:41], v[46:47], v[26:27], v[40:41] op_sel:[0,1,0]
	v_pk_fma_f32 v[6:7], v[48:49], v[26:27], v[6:7] op_sel:[0,1,0]
	v_mov_b32_e32 v4, v29
	s_waitcnt vmcnt(4)
	v_cvt_f32_f16_e32 v26, v32
	v_cvt_f32_f16_sdwa v27, v32 dst_sel:DWORD dst_unused:UNUSED_PAD src0_sel:WORD_1
	v_cvt_f32_f16_e32 v28, v33
	v_cvt_f32_f16_sdwa v29, v33 dst_sel:DWORD dst_unused:UNUSED_PAD src0_sel:WORD_1
	v_cvt_f32_f16_e32 v32, v34
	v_cvt_f32_f16_sdwa v33, v34 dst_sel:DWORD dst_unused:UNUSED_PAD src0_sel:WORD_1
	v_cvt_f32_f16_e32 v34, v35
	v_cvt_f32_f16_sdwa v35, v35 dst_sel:DWORD dst_unused:UNUSED_PAD src0_sel:WORD_1
	v_pk_fma_f32 v[8:9], v[26:27], v[4:5], v[8:9] op_sel_hi:[1,0,1]
	v_pk_fma_f32 v[26:27], v[28:29], v[4:5], v[30:31] op_sel_hi:[1,0,1]
	v_pk_fma_f32 v[28:29], v[32:33], v[4:5], v[40:41] op_sel_hi:[1,0,1]
	v_pk_fma_f32 v[6:7], v[34:35], v[4:5], v[6:7] op_sel_hi:[1,0,1]
	s_waitcnt vmcnt(3)
	v_cvt_f32_f16_e32 v30, v36
	v_cvt_f32_f16_sdwa v31, v36 dst_sel:DWORD dst_unused:UNUSED_PAD src0_sel:WORD_1
	v_cvt_f32_f16_e32 v32, v37
	v_cvt_f32_f16_sdwa v33, v37 dst_sel:DWORD dst_unused:UNUSED_PAD src0_sel:WORD_1
	v_cvt_f32_f16_e32 v34, v38
	v_cvt_f32_f16_sdwa v35, v38 dst_sel:DWORD dst_unused:UNUSED_PAD src0_sel:WORD_1
	v_cvt_f32_f16_e32 v36, v39
	v_cvt_f32_f16_sdwa v37, v39 dst_sel:DWORD dst_unused:UNUSED_PAD src0_sel:WORD_1
	v_pk_fma_f32 v[8:9], v[30:31], v[10:11], v[8:9] op_sel:[0,1,0]
	v_pk_fma_f32 v[26:27], v[32:33], v[10:11], v[26:27] op_sel:[0,1,0]
	v_pk_fma_f32 v[28:29], v[34:35], v[10:11], v[28:29] op_sel:[0,1,0]
	v_pk_fma_f32 v[6:7], v[36:37], v[10:11], v[6:7] op_sel:[0,1,0]
	v_mov_b32_e32 v4, v13
	s_waitcnt vmcnt(2)
	v_cvt_f32_f16_e32 v10, v18
	v_cvt_f32_f16_sdwa v11, v18 dst_sel:DWORD dst_unused:UNUSED_PAD src0_sel:WORD_1
	v_cvt_f32_f16_e32 v12, v19
	v_cvt_f32_f16_sdwa v13, v19 dst_sel:DWORD dst_unused:UNUSED_PAD src0_sel:WORD_1
	v_cvt_f32_f16_e32 v18, v20
	v_cvt_f32_f16_sdwa v19, v20 dst_sel:DWORD dst_unused:UNUSED_PAD src0_sel:WORD_1
	v_cvt_f32_f16_e32 v20, v21
	v_cvt_f32_f16_sdwa v21, v21 dst_sel:DWORD dst_unused:UNUSED_PAD src0_sel:WORD_1
	v_pk_fma_f32 v[8:9], v[10:11], v[4:5], v[8:9] op_sel_hi:[1,0,1]
	v_pk_fma_f32 v[10:11], v[12:13], v[4:5], v[26:27] op_sel_hi:[1,0,1]
	v_pk_fma_f32 v[12:13], v[18:19], v[4:5], v[28:29] op_sel_hi:[1,0,1]
	v_pk_fma_f32 v[6:7], v[20:21], v[4:5], v[6:7] op_sel_hi:[1,0,1]
	s_waitcnt vmcnt(1)
	v_cvt_f32_f16_e32 v18, v22
	v_cvt_f32_f16_sdwa v19, v22 dst_sel:DWORD dst_unused:UNUSED_PAD src0_sel:WORD_1
	v_cvt_f32_f16_e32 v20, v23
	v_cvt_f32_f16_sdwa v21, v23 dst_sel:DWORD dst_unused:UNUSED_PAD src0_sel:WORD_1
	v_cvt_f32_f16_e32 v22, v24
	v_cvt_f32_f16_sdwa v23, v24 dst_sel:DWORD dst_unused:UNUSED_PAD src0_sel:WORD_1
	v_cvt_f32_f16_e32 v24, v25
	v_cvt_f32_f16_sdwa v25, v25 dst_sel:DWORD dst_unused:UNUSED_PAD src0_sel:WORD_1
	v_pk_fma_f32 v[8:9], v[18:19], v[2:3], v[8:9] op_sel:[0,1,0]
	v_pk_fma_f32 v[10:11], v[20:21], v[2:3], v[10:11] op_sel:[0,1,0]
	v_pk_fma_f32 v[12:13], v[22:23], v[2:3], v[12:13] op_sel:[0,1,0]
	v_pk_fma_f32 v[2:3], v[24:25], v[2:3], v[6:7] op_sel:[0,1,0]
	s_waitcnt vmcnt(0)
	v_cvt_f32_f16_e32 v6, v14
	v_cvt_f32_f16_sdwa v7, v14 dst_sel:DWORD dst_unused:UNUSED_PAD src0_sel:WORD_1
	v_cvt_f32_f16_e32 v14, v15
	v_cvt_f32_f16_sdwa v15, v15 dst_sel:DWORD dst_unused:UNUSED_PAD src0_sel:WORD_1
	v_cvt_f32_f16_e32 v18, v16
	v_cvt_f32_f16_sdwa v19, v16 dst_sel:DWORD dst_unused:UNUSED_PAD src0_sel:WORD_1
	v_cvt_f32_f16_e32 v16, v17
	v_cvt_f32_f16_sdwa v17, v17 dst_sel:DWORD dst_unused:UNUSED_PAD src0_sel:WORD_1
	v_mov_b32_e32 v4, v5
	v_pk_fma_f32 v[110:111], v[6:7], v[4:5], v[8:9] op_sel_hi:[1,0,1]
	v_pk_fma_f32 v[112:113], v[14:15], v[4:5], v[10:11] op_sel_hi:[1,0,1]
	v_pk_fma_f32 v[114:115], v[18:19], v[4:5], v[12:13] op_sel_hi:[1,0,1]
	v_pk_fma_f32 v[108:109], v[16:17], v[4:5], v[2:3] op_sel_hi:[1,0,1]

.LBB4_28:
	s_or_b64 exec, exec, s[18:19]
	s_mov_b64 s[4:5], s[44:45]
	s_mov_b64 s[6:7], s[46:47]
	s_mov_b64 s[16:17], s[48:49]
	v_cndmask_b32_e64 v8, 0, v98, s[2:3]
	v_ashrrev_i32_e32 v9, 31, v8
	v_lshlrev_b64 v[2:3], 8, v[8:9]
	v_mov_b32_e32 v101, 0
	s_waitcnt lgkmcnt(0)
	v_lshl_add_u64 v[2:3], s[16:17], 0, v[2:3]
	v_lshl_add_u64 v[2:3], v[2:3], 0, v[100:101]
	global_load_dwordx4 v[2:5], v[2:3], off
	v_ashrrev_i32_e32 v18, 5, v8
	v_lshl_add_u64 v[8:9], v[8:9], 2, s[10:11]
	v_ashrrev_i32_e32 v19, 31, v18
	global_load_dword v22, v[8:9], off
	v_lshl_add_u64 v[8:9], v[18:19], 2, s[8:9]
	global_load_dword v8, v[8:9], off
	v_pk_mul_f32 v[10:11], v[110:111], v[110:111]
	v_pk_mul_f32 v[12:13], v[112:113], v[112:113]
	v_add_f32_e32 v10, v10, v11
	v_add_f32_e32 v10, v10, v12
	v_pk_mul_f32 v[14:15], v[114:115], v[114:115]
	v_add_f32_e32 v10, v10, v13
	v_max3_f32 v7, |v110|, 0, |v111|
	v_xor_b32_e32 v20, 1, v119
	v_add_f32_e32 v10, v10, v14
	v_pk_mul_f32 v[16:17], v[108:109], v[108:109]
	v_max3_f32 v7, v7, |v112|, |v113|
	v_cmp_lt_i32_e32 vcc, v20, v120
	v_add_f32_e32 v10, v10, v15
	v_max3_f32 v7, v7, |v114|, |v115|
	v_cndmask_b32_e32 v11, v119, v20, vcc
	v_add_f32_e32 v10, v10, v16
	v_lshlrev_b32_e32 v11, 2, v11
	v_max3_f32 v7, v7, |v108|, |v109|
	v_add_f32_e32 v10, v10, v17
	ds_bpermute_b32 v12, v11, v7
	ds_bpermute_b32 v13, v11, v10
	v_xor_b32_e32 v21, 2, v119
	v_cmp_lt_i32_e32 vcc, v21, v120
	v_xor_b32_e32 v9, 4, v119
	s_waitcnt lgkmcnt(1)
	v_max_f32_e32 v12, v12, v12
	v_cndmask_b32_e32 v19, v119, v21, vcc
	v_lshlrev_b32_e32 v14, 2, v19
	s_waitcnt lgkmcnt(0)
	v_add_f32_e32 v10, v10, v13
	v_max_f32_e32 v7, v7, v12
	ds_bpermute_b32 v12, v14, v10
	v_cmp_lt_i32_e32 vcc, v9, v120
	ds_bpermute_b32 v13, v14, v7
	v_xor_b32_e32 v18, 8, v119
	v_cndmask_b32_e32 v9, v119, v9, vcc
	v_lshlrev_b32_e32 v9, 2, v9
	s_waitcnt lgkmcnt(1)
	v_add_f32_e32 v10, v10, v12
	ds_bpermute_b32 v12, v9, v10
	v_cmp_lt_i32_e32 vcc, v18, v120
	s_waitcnt lgkmcnt(1)
	v_max_f32_e32 v13, v13, v13
	v_max_f32_e32 v7, v7, v13
	v_cndmask_b32_e32 v15, v119, v18, vcc
	v_lshlrev_b32_e32 v15, 2, v15
	s_waitcnt lgkmcnt(0)
	v_add_f32_e32 v10, v10, v12
	ds_bpermute_b32 v12, v15, v10
	ds_bpermute_b32 v13, v9, v7
	s_mov_b32 s0, 0xf800000
	v_and_b32_e32 v6, 63, v0
	s_waitcnt lgkmcnt(1)
	v_add_f32_e32 v10, v10, v12
	s_waitcnt lgkmcnt(0)
	v_max_f32_e32 v13, v13, v13
	v_mul_f32_e32 v12, 0x4f800000, v10
	v_cmp_gt_f32_e32 vcc, s0, v10
	v_max_f32_e32 v7, v7, v13
	ds_bpermute_b32 v13, v15, v7
	v_cndmask_b32_e32 v10, v10, v12, vcc
	v_sqrt_f32_e32 v12, v10
	s_waitcnt vmcnt(2)
	v_fma_mix_f32 v16, v110, v2, 0 op_sel_hi:[0,1,0]
	v_fma_mix_f32 v2, v111, v2, v16 op_sel:[0,1,0] op_sel_hi:[0,1,0]
	v_fma_mix_f32 v2, v112, v3, v2 op_sel_hi:[0,1,0]
	v_fma_mix_f32 v2, v113, v3, v2 op_sel:[0,1,0] op_sel_hi:[0,1,0]
	v_fma_mix_f32 v2, v114, v4, v2 op_sel_hi:[0,1,0]
	v_fma_mix_f32 v2, v115, v4, v2 op_sel:[0,1,0] op_sel_hi:[0,1,0]
	v_fma_mix_f32 v2, v108, v5, v2 op_sel_hi:[0,1,0]
	v_fma_mix_f32 v2, v109, v5, v2 op_sel:[0,1,0] op_sel_hi:[0,1,0]
	ds_bpermute_b32 v3, v11, v2
	v_add_u32_e32 v11, -1, v12
	s_waitcnt lgkmcnt(1)
	v_max_f32_e32 v5, v13, v13
	v_add_u32_e32 v13, 1, v12
	v_fma_f32 v16, -v13, v12, v10
	s_waitcnt lgkmcnt(0)
	v_add_f32_e32 v2, v2, v3
	ds_bpermute_b32 v3, v14, v2
	v_fma_f32 v14, -v11, v12, v10
	v_cmp_ge_f32_e64 s[0:1], 0, v14
	v_mov_b32_e32 v4, 0x260
	v_max_f32_e32 v5, v7, v5
	s_waitcnt lgkmcnt(0)
	v_add_f32_e32 v2, v2, v3
	ds_bpermute_b32 v3, v9, v2
	v_cndmask_b32_e64 v11, v12, v11, s[0:1]
	v_cmp_lt_f32_e64 s[0:1], 0, v16
	s_waitcnt lgkmcnt(0)
	v_add_f32_e32 v2, v2, v3
	ds_bpermute_b32 v3, v15, v2
	v_cndmask_b32_e64 v9, v11, v13, s[0:1]
	v_mul_f32_e32 v11, 0x37800000, v9
	v_cndmask_b32_e32 v9, v9, v11, vcc
	v_cmp_class_f32_e32 vcc, v10, v4
	s_waitcnt lgkmcnt(0)
	v_add_f32_e32 v2, v2, v3
	s_waitcnt vmcnt(0)
	v_mul_f32_e32 v2, v8, v2
	v_cndmask_b32_e32 v4, v9, v10, vcc
	v_max_f32_e32 v4, 0x322bcc77, v4
	v_mul_f32_e32 v4, v22, v4
	v_div_scale_f32 v3, s[0:1], v4, v4, v2
	v_rcp_f32_e32 v8, v3
	v_div_scale_f32 v7, vcc, v2, v4, v2
	v_fma_f32 v9, -v3, v8, 1.0
	v_fmac_f32_e32 v8, v9, v8
	v_mul_f32_e32 v9, v7, v8
	v_fma_f32 v10, -v3, v9, v7
	v_fmac_f32_e32 v9, v10, v8
	v_fma_f32 v3, -v3, v9, v7
	v_div_fmas_f32 v3, v3, v8, v9
	v_div_fixup_f32 v2, v3, v4, v2
	v_mul_f32_e64 v3, v5, |v2|
	v_cndmask_b32_e64 v3, 0, v3, s[2:3]
	ds_bpermute_b32 v4, v117, v3
	v_cmp_eq_u32_e32 vcc, 0, v6
	s_waitcnt lgkmcnt(0)
	v_max_f32_e32 v4, v4, v4
	v_max_f32_e32 v3, v3, v4
	ds_bpermute_b32 v4, v118, v3
	s_and_saveexec_b64 s[0:1], vcc
	s_cbranch_execz .LBB4_30
	s_waitcnt lgkmcnt(0)
	v_max_f32_e32 v4, v4, v4
	v_max_f32_e32 v3, v3, v3
	v_max_f32_e32 v3, v3, v4
	ds_write_b32 v1, v3 offset:16384

	.amdhsa_kernel _Z6k_spmmILb0ELi0EEvPKiPK15HIP_vector_typeIiLj2EEPKvPKfPKDF16_S9_S9_iPfPDF16_PhSC_PKhS9_SG_S9_S9_i
		.amdhsa_group_segment_fixed_size 20544
		.amdhsa_private_segment_fixed_size 0
		.amdhsa_kernarg_size 400
		.amdhsa_user_sgpr_count 2
		.amdhsa_user_sgpr_dispatch_ptr 0
		.amdhsa_user_sgpr_queue_ptr 0
		.amdhsa_user_sgpr_kernarg_segment_ptr 1
		.amdhsa_user_sgpr_dispatch_id 0
		.amdhsa_user_sgpr_kernarg_preload_length 0
		.amdhsa_user_sgpr_kernarg_preload_offset 0
		.amdhsa_user_sgpr_private_segment_size 0
		.amdhsa_uses_dynamic_stack 0
		.amdhsa_enable_private_segment 0
		.amdhsa_system_sgpr_workgroup_id_x 1
		.amdhsa_system_sgpr_workgroup_id_y 0
		.amdhsa_system_sgpr_workgroup_id_z 0
		.amdhsa_system_sgpr_workgroup_info 0
		.amdhsa_system_vgpr_workitem_id 0
		.amdhsa_next_free_vgpr 128
		.amdhsa_next_free_sgpr 50
		.amdhsa_accum_offset 128
		.amdhsa_reserve_vcc 1
		.amdhsa_float_round_mode_32 0
		.amdhsa_float_round_mode_16_64 0
		.amdhsa_float_denorm_mode_32 3
		.amdhsa_float_denorm_mode_16_64 3
		.amdhsa_dx10_clamp 1
		.amdhsa_ieee_mode 1
		.amdhsa_fp16_overflow 0
		.amdhsa_tg_split 0
		.amdhsa_exception_fp_ieee_invalid_op 0
		.amdhsa_exception_fp_denorm_src 0
		.amdhsa_exception_fp_ieee_div_zero 0
		.amdhsa_exception_fp_ieee_overflow 0
		.amdhsa_exception_fp_ieee_underflow 0
		.amdhsa_exception_fp_ieee_inexact 0
		.amdhsa_exception_int_div_zero 0
	.end_amdhsa_kernel

_Z6k_spmmILb1ELi1EEvPKiPK15HIP_vector_typeIiLj2EEPKvPKfPKDF16_S9_S9_iPfPDF16_PhSC_PKhS9_SG_S9_S9_i:
	s_load_dword s3, s[0:1], 0x90
	s_load_dwordx2 s[40:41], s[0:1], 0x10
	s_load_dwordx2 s[42:43], s[0:1], 0x50
	s_load_dwordx2 s[44:45], s[0:1], 0x20
	s_load_dwordx2 s[8:9], s[0:1], 0x0
	s_load_dwordx2 s[14:15], s[0:1], 0x8
	s_load_dword s4, s[0:1], 0x38
	s_not_b32 s2, s2
	v_lshrrev_b32_e32 v2, 4, v0
	s_waitcnt lgkmcnt(0)
	s_add_i32 s6, s3, s2
	v_bfe_u32 v1, v0, 4, 2
	s_lshl_b32 s2, s6, 5
	v_and_b32_e32 v2, 28, v2
	s_nop 0
	v_mbcnt_lo_u32_b32 v5, -1, 0
	v_mbcnt_hi_u32_b32 v5, -1, v5
	v_min_u32_e32 v6, 32, v5
	v_add_u32_e32 v6, s2, v6
	v_min_i32_e32 v6, s4, v6
	v_lshlrev_b32_e32 v7, 2, v6
	v_lshrrev_b32_e32 v9, 6, v0
	v_lshlrev_b32_e32 v9, 9, v9
	v_lshlrev_b32_e32 v10, 2, v5
	v_add_u32_e32 v11, v9, v10
	s_waitcnt lgkmcnt(0)
	global_load_dword v8, v7, s[8:9]
	v_cmp_gt_u32_e32 vcc, 33, v5
	s_waitcnt vmcnt(0)
	s_and_saveexec_b64 s[10:11], vcc
	ds_write_b32 v11, v8 offset:16448
	s_mov_b64 exec, s[10:11]
	ds_read_b32 v12, v11 offset:16452
	v_sub_u32_e32 v13, 31, v5
	s_waitcnt lgkmcnt(0)
	v_sub_u32_e32 v12, v12, v8
	v_lshl_add_u32 v12, v12, 5, v13
	v_cmp_gt_u32_e32 vcc, 32, v5
	s_and_saveexec_b64 s[10:11], vcc
	ds_write_b32 v11, v12 offset:16608
	s_mov_b64 exec, s[10:11]
	v_mov_b32_e32 v13, 0
	ds_read_b128 v[14:17], v9 offset:16608
	s_waitcnt lgkmcnt(0)
	v_sub_u32_e32 v6, v12, v14
	v_ashrrev_i32_e32 v6, 31, v6
	v_sub_u32_e32 v13, v13, v6
	v_sub_u32_e32 v6, v12, v15
	v_ashrrev_i32_e32 v6, 31, v6
	v_sub_u32_e32 v13, v13, v6
	v_sub_u32_e32 v6, v12, v16
	v_ashrrev_i32_e32 v6, 31, v6
	v_sub_u32_e32 v13, v13, v6
	v_sub_u32_e32 v6, v12, v17
	v_ashrrev_i32_e32 v6, 31, v6
	v_sub_u32_e32 v13, v13, v6
	ds_read_b128 v[14:17], v9 offset:16624
	s_waitcnt lgkmcnt(0)
	v_sub_u32_e32 v6, v12, v14
	v_ashrrev_i32_e32 v6, 31, v6
	v_sub_u32_e32 v13, v13, v6
	v_sub_u32_e32 v6, v12, v15
	v_ashrrev_i32_e32 v6, 31, v6
	v_sub_u32_e32 v13, v13, v6
	v_sub_u32_e32 v6, v12, v16
	v_ashrrev_i32_e32 v6, 31, v6
	v_sub_u32_e32 v13, v13, v6
	v_sub_u32_e32 v6, v12, v17
	v_ashrrev_i32_e32 v6, 31, v6
	v_sub_u32_e32 v13, v13, v6
	ds_read_b128 v[14:17], v9 offset:16640
	s_waitcnt lgkmcnt(0)
	v_sub_u32_e32 v6, v12, v14
	v_ashrrev_i32_e32 v6, 31, v6
	v_sub_u32_e32 v13, v13, v6
	v_sub_u32_e32 v6, v12, v15
	v_ashrrev_i32_e32 v6, 31, v6
	v_sub_u32_e32 v13, v13, v6
	v_sub_u32_e32 v6, v12, v16
	v_ashrrev_i32_e32 v6, 31, v6
	v_sub_u32_e32 v13, v13, v6
	v_sub_u32_e32 v6, v12, v17
	v_ashrrev_i32_e32 v6, 31, v6
	v_sub_u32_e32 v13, v13, v6
	ds_read_b128 v[14:17], v9 offset:16656
	s_waitcnt lgkmcnt(0)
	v_sub_u32_e32 v6, v12, v14
	v_ashrrev_i32_e32 v6, 31, v6
	v_sub_u32_e32 v13, v13, v6
	v_sub_u32_e32 v6, v12, v15
	v_ashrrev_i32_e32 v6, 31, v6
	v_sub_u32_e32 v13, v13, v6
	v_sub_u32_e32 v6, v12, v16
	v_ashrrev_i32_e32 v6, 31, v6
	v_sub_u32_e32 v13, v13, v6
	v_sub_u32_e32 v6, v12, v17
	v_ashrrev_i32_e32 v6, 31, v6
	v_sub_u32_e32 v13, v13, v6
	ds_read_b128 v[14:17], v9 offset:16672
	s_waitcnt lgkmcnt(0)
	v_sub_u32_e32 v6, v12, v14
	v_ashrrev_i32_e32 v6, 31, v6
	v_sub_u32_e32 v13, v13, v6
	v_sub_u32_e32 v6, v12, v15
	v_ashrrev_i32_e32 v6, 31, v6
	v_sub_u32_e32 v13, v13, v6
	v_sub_u32_e32 v6, v12, v16
	v_ashrrev_i32_e32 v6, 31, v6
	v_sub_u32_e32 v13, v13, v6
	v_sub_u32_e32 v6, v12, v17
	v_ashrrev_i32_e32 v6, 31, v6
	v_sub_u32_e32 v13, v13, v6
	ds_read_b128 v[14:17], v9 offset:16688
	s_waitcnt lgkmcnt(0)
	v_sub_u32_e32 v6, v12, v14
	v_ashrrev_i32_e32 v6, 31, v6
	v_sub_u32_e32 v13, v13, v6
	v_sub_u32_e32 v6, v12, v15
	v_ashrrev_i32_e32 v6, 31, v6
	v_sub_u32_e32 v13, v13, v6
	v_sub_u32_e32 v6, v12, v16
	v_ashrrev_i32_e32 v6, 31, v6
	v_sub_u32_e32 v13, v13, v6
	v_sub_u32_e32 v6, v12, v17
	v_ashrrev_i32_e32 v6, 31, v6
	v_sub_u32_e32 v13, v13, v6
	ds_read_b128 v[14:17], v9 offset:16704
	s_waitcnt lgkmcnt(0)
	v_sub_u32_e32 v6, v12, v14
	v_ashrrev_i32_e32 v6, 31, v6
	v_sub_u32_e32 v13, v13, v6
	v_sub_u32_e32 v6, v12, v15
	v_ashrrev_i32_e32 v6, 31, v6
	v_sub_u32_e32 v13, v13, v6
	v_sub_u32_e32 v6, v12, v16
	v_ashrrev_i32_e32 v6, 31, v6
	v_sub_u32_e32 v13, v13, v6
	v_sub_u32_e32 v6, v12, v17
	v_ashrrev_i32_e32 v6, 31, v6
	v_sub_u32_e32 v13, v13, v6
	ds_read_b128 v[14:17], v9 offset:16720
	s_waitcnt lgkmcnt(0)
	v_sub_u32_e32 v6, v12, v14
	v_ashrrev_i32_e32 v6, 31, v6
	v_sub_u32_e32 v13, v13, v6
	v_sub_u32_e32 v6, v12, v15
	v_ashrrev_i32_e32 v6, 31, v6
	v_sub_u32_e32 v13, v13, v6
	v_sub_u32_e32 v6, v12, v16
	v_ashrrev_i32_e32 v6, 31, v6
	v_sub_u32_e32 v13, v13, v6
	v_sub_u32_e32 v6, v12, v17
	v_ashrrev_i32_e32 v6, 31, v6
	v_sub_u32_e32 v13, v13, v6
	v_lshl_add_u32 v6, v13, 2, v9
	v_cmp_gt_u32_e32 vcc, 32, v5
	s_and_saveexec_b64 s[10:11], vcc
	ds_write_b32 v6, v5 offset:16768
	s_mov_b64 exec, s[10:11]
	v_bfe_u32 v6, v0, 4, 5
	v_lshl_add_u32 v6, v6, 2, v9
	ds_read_b32 v7, v6 offset:16768
	s_waitcnt lgkmcnt(0)
	v_add_u32_e32 v18, s2, v7
	v_lshl_add_u32 v7, v7, 2, v9
	ds_read_b32 v4, v7 offset:16448
	ds_read_b32 v6, v7 offset:16452
	v_ashrrev_i32_e32 v19, 31, v18
	v_mov_b32_e32 v2, 0
	s_waitcnt lgkmcnt(0)
	v_sub_u32_e32 v55, v6, v4
	v_cmp_gt_i32_e64 s[2:3], s4, v18
	s_mov_b64 s[4:5], exec
	s_nop 1
	v_cndmask_b32_e64 v4, 0, v4, s[2:3]
	v_cndmask_b32_e64 v55, 0, v55, s[2:3]

.LBB5_10:
	s_or_b64 exec, exec, s[4:5]
	s_waitcnt vmcnt(0)
	v_ashrrev_i32_e32 v12, 5, v2
	v_ashrrev_i32_e32 v13, 31, v12
	v_ashrrev_i32_e32 v14, 5, v6
	v_ashrrev_i32_e32 v16, 5, v4
	v_ashrrev_i32_e32 v24, 5, v8
	s_waitcnt lgkmcnt(0)
	v_lshl_add_u64 v[12:13], v[12:13], 2, s[16:17]
	v_ashrrev_i32_e32 v15, 31, v14
	v_ashrrev_i32_e32 v17, 31, v16
	v_ashrrev_i32_e32 v25, 31, v24
	v_lshl_add_u64 v[14:15], v[14:15], 2, s[16:17]
	v_lshl_add_u64 v[16:17], v[16:17], 2, s[16:17]
	v_lshl_add_u64 v[24:25], v[24:25], 2, s[16:17]
	global_load_dword v26, v[12:13], off
	global_load_dword v27, v[14:15], off
	s_nop 0
	global_load_dword v12, v[16:17], off
	global_load_dword v13, v[24:25], off
	s_load_dwordx2 s[12:13], s[0:1], 0x58
	s_load_dwordx4 s[8:11], s[0:1], 0x28
	v_lshlrev_b32_e32 v1, 5, v0
	v_max_i32_e32 v23, v10, v11
	v_lshlrev_b32_e32 v20, 3, v56
	v_and_b32_e32 v57, 0x3e00, v1
	v_mov_b32_e32 v34, 0
	v_mov_b32_e32 v33, 0
	v_mov_b32_e32 v32, 0
	v_mov_b32_e32 v31, 0
	v_mov_b32_e32 v30, 0
	v_mov_b32_e32 v29, 0
	v_cmp_lt_i32_e32 vcc, 0, v23
	v_or_b32_e32 v1, v57, v20
	v_mov_b32_e32 v28, 0
	s_waitcnt vmcnt(3)
	v_mul_f32_e32 v3, v3, v26
	s_waitcnt vmcnt(2)
	v_mul_f32_e32 v7, v7, v27
	s_waitcnt vmcnt(1)
	v_mul_f32_e32 v5, v5, v12
	s_waitcnt vmcnt(0)
	v_mul_f32_e32 v9, v9, v13
	ds_write2_b64 v1, v[2:3], v[6:7] offset1:16
	ds_write2_b64 v1, v[4:5], v[8:9] offset0:32 offset1:48
	s_and_saveexec_b64 s[18:19], vcc
	s_cbranch_execz .LBB5_36
	s_mov_b64 s[20:21], s[40:41]
	ds_read_b128 v[14:17], v57
	ds_read_b128 v[10:13], v57 offset:16
	ds_read_b128 v[6:9], v57 offset:32
	ds_read_b128 v[2:5], v57 offset:48
	v_cmp_lt_u32_e32 vcc, 8, v23
	s_waitcnt lgkmcnt(0)
	v_lshl_or_b32 v24, v14, 7, v20
	v_lshl_or_b32 v16, v16, 7, v20
	global_load_dwordx2 v[38:39], v24, s[20:21]
	global_load_dwordx2 v[36:37], v16, s[20:21]
	v_lshl_or_b32 v12, v12, 7, v20
	global_load_dwordx2 v[30:31], v12, s[20:21]
	v_lshl_or_b32 v16, v10, 7, v20
	global_load_dwordx2 v[34:35], v16, s[20:21]
	v_lshl_or_b32 v8, v8, 7, v20
	global_load_dwordx2 v[28:29], v8, s[20:21]
	v_lshl_or_b32 v12, v6, 7, v20
	global_load_dwordx2 v[32:33], v12, s[20:21]
	v_lshl_or_b32 v4, v4, 7, v20
	global_load_dwordx2 v[24:25], v4, s[20:21]
	v_lshl_or_b32 v8, v2, 7, v20
	global_load_dwordx2 v[26:27], v8, s[20:21]
	v_mov_b32_e32 v4, v17
	s_waitcnt vmcnt(7)
	v_cvt_pk_f32_fp8_e32 v[40:41], v38
	v_cvt_pk_f32_fp8_sdwa v[42:43], v38 src0_sel:WORD_1
	v_cvt_pk_f32_fp8_e32 v[44:45], v39
	v_cvt_pk_f32_fp8_sdwa v[38:39], v39 src0_sel:WORD_1
	s_waitcnt vmcnt(6)
	v_cvt_pk_f32_fp8_e32 v[16:17], v36
	v_pk_fma_f32 v[40:41], v[40:41], v[14:15], 0 op_sel:[0,1,0] op_sel_hi:[1,1,0]
	v_pk_fma_f32 v[42:43], v[42:43], v[14:15], 0 op_sel:[0,1,0] op_sel_hi:[1,1,0]
	v_pk_fma_f32 v[44:45], v[44:45], v[14:15], 0 op_sel:[0,1,0] op_sel_hi:[1,1,0]
	v_pk_fma_f32 v[14:15], v[38:39], v[14:15], 0 op_sel:[0,1,0] op_sel_hi:[1,1,0]
	v_pk_fma_f32 v[16:17], v[16:17], v[4:5], v[40:41] op_sel_hi:[1,0,1]
	v_cvt_pk_f32_fp8_sdwa v[38:39], v36 src0_sel:WORD_1
	v_cvt_pk_f32_fp8_e32 v[40:41], v37
	v_cvt_pk_f32_fp8_sdwa v[36:37], v37 src0_sel:WORD_1
	v_pk_fma_f32 v[38:39], v[38:39], v[4:5], v[42:43] op_sel_hi:[1,0,1]
	v_pk_fma_f32 v[40:41], v[40:41], v[4:5], v[44:45] op_sel_hi:[1,0,1]
	v_pk_fma_f32 v[14:15], v[36:37], v[4:5], v[14:15] op_sel_hi:[1,0,1]
	s_waitcnt vmcnt(4)
	v_cvt_pk_f32_fp8_e32 v[36:37], v34
	v_mov_b32_e32 v4, v13
	v_cvt_pk_f32_fp8_e32 v[12:13], v30
	v_pk_fma_f32 v[16:17], v[36:37], v[10:11], v[16:17] op_sel:[0,1,0]
	v_cvt_pk_f32_fp8_sdwa v[36:37], v34 src0_sel:WORD_1
	v_pk_fma_f32 v[12:13], v[12:13], v[4:5], v[16:17] op_sel_hi:[1,0,1]
	v_cvt_pk_f32_fp8_e32 v[16:17], v31
	v_pk_fma_f32 v[36:37], v[36:37], v[10:11], v[38:39] op_sel:[0,1,0]
	v_cvt_pk_f32_fp8_e32 v[38:39], v35
	v_cvt_pk_f32_fp8_sdwa v[34:35], v35 src0_sel:WORD_1
	v_pk_fma_f32 v[38:39], v[38:39], v[10:11], v[40:41] op_sel:[0,1,0]
	v_pk_fma_f32 v[10:11], v[34:35], v[10:11], v[14:15] op_sel:[0,1,0]
	v_cvt_pk_f32_fp8_sdwa v[14:15], v30 src0_sel:WORD_1
	v_cvt_pk_f32_fp8_sdwa v[30:31], v31 src0_sel:WORD_1
	v_pk_fma_f32 v[16:17], v[16:17], v[4:5], v[38:39] op_sel_hi:[1,0,1]
	v_pk_fma_f32 v[14:15], v[14:15], v[4:5], v[36:37] op_sel_hi:[1,0,1]
	v_pk_fma_f32 v[10:11], v[30:31], v[4:5], v[10:11] op_sel_hi:[1,0,1]
	s_waitcnt vmcnt(2)
	v_cvt_pk_f32_fp8_e32 v[30:31], v32
	v_mov_b32_e32 v4, v9
	v_cvt_pk_f32_fp8_e32 v[8:9], v28
	v_pk_fma_f32 v[12:13], v[30:31], v[6:7], v[12:13] op_sel:[0,1,0]
	v_cvt_pk_f32_fp8_sdwa v[30:31], v32 src0_sel:WORD_1
	v_pk_fma_f32 v[8:9], v[8:9], v[4:5], v[12:13] op_sel_hi:[1,0,1]
	v_pk_fma_f32 v[14:15], v[30:31], v[6:7], v[14:15] op_sel:[0,1,0]
	v_cvt_pk_f32_fp8_e32 v[30:31], v33
	v_pk_fma_f32 v[16:17], v[30:31], v[6:7], v[16:17] op_sel:[0,1,0]
	v_cvt_pk_f32_fp8_sdwa v[30:31], v33 src0_sel:WORD_1
	v_pk_fma_f32 v[6:7], v[30:31], v[6:7], v[10:11] op_sel:[0,1,0]
	v_cvt_pk_f32_fp8_sdwa v[10:11], v28 src0_sel:WORD_1
	v_pk_fma_f32 v[12:13], v[10:11], v[4:5], v[14:15] op_sel_hi:[1,0,1]
	v_cvt_pk_f32_fp8_e32 v[10:11], v29
	v_pk_fma_f32 v[14:15], v[10:11], v[4:5], v[16:17] op_sel_hi:[1,0,1]
	v_cvt_pk_f32_fp8_sdwa v[10:11], v29 src0_sel:WORD_1
	v_pk_fma_f32 v[16:17], v[10:11], v[4:5], v[6:7] op_sel_hi:[1,0,1]
	s_waitcnt vmcnt(0)
	v_cvt_pk_f32_fp8_e32 v[6:7], v26
	v_mov_b32_e32 v4, v5
	v_pk_fma_f32 v[10:11], v[6:7], v[2:3], v[8:9] op_sel:[0,1,0]
	v_cvt_pk_f32_fp8_sdwa v[6:7], v26 src0_sel:WORD_1
	v_pk_fma_f32 v[8:9], v[6:7], v[2:3], v[12:13] op_sel:[0,1,0]
	v_cvt_pk_f32_fp8_e32 v[6:7], v27
	v_cvt_pk_f32_fp8_sdwa v[12:13], v27 src0_sel:WORD_1
	v_pk_fma_f32 v[6:7], v[6:7], v[2:3], v[14:15] op_sel:[0,1,0]
	v_pk_fma_f32 v[2:3], v[12:13], v[2:3], v[16:17] op_sel:[0,1,0]
	v_cvt_pk_f32_fp8_e32 v[12:13], v24
	v_pk_fma_f32 v[28:29], v[12:13], v[4:5], v[10:11] op_sel_hi:[1,0,1]
	v_cvt_pk_f32_fp8_sdwa v[10:11], v24 src0_sel:WORD_1
	v_pk_fma_f32 v[30:31], v[10:11], v[4:5], v[8:9] op_sel_hi:[1,0,1]
	v_cvt_pk_f32_fp8_e32 v[8:9], v25
	v_pk_fma_f32 v[32:33], v[8:9], v[4:5], v[6:7] op_sel_hi:[1,0,1]
	v_cvt_pk_f32_fp8_sdwa v[6:7], v25 src0_sel:WORD_1
	v_pk_fma_f32 v[34:35], v[6:7], v[4:5], v[2:3] op_sel_hi:[1,0,1]
	s_and_saveexec_b64 s[4:5], vcc
	s_cbranch_execnz .LBB5_15
	s_or_b64 exec, exec, s[4:5]
	v_cmp_lt_u32_e32 vcc, 16, v23
	s_and_saveexec_b64 s[4:5], vcc
	s_cbranch_execnz .LBB5_16

.LBB5_36:
	s_or_b64 exec, exec, s[18:19]
	s_mov_b64 s[4:5], s[42:43]
	s_mov_b64 s[14:15], s[44:45]
	v_cndmask_b32_e64 v10, 0, v18, s[2:3]
	v_ashrrev_i32_e32 v11, 31, v10
	v_lshlrev_b64 v[2:3], 8, v[10:11]
	v_mov_b32_e32 v7, 0
	s_waitcnt lgkmcnt(0)
	v_lshl_add_u64 v[2:3], s[14:15], 0, v[2:3]
	v_lshlrev_b32_e32 v6, 1, v20
	v_lshl_add_u64 v[2:3], v[2:3], 0, v[6:7]
	global_load_dwordx4 v[2:5], v[2:3], off
	v_ashrrev_i32_e32 v12, 5, v10
	v_lshl_add_u64 v[10:11], v[10:11], 2, s[10:11]
	v_ashrrev_i32_e32 v13, 31, v12
	global_load_dword v15, v[10:11], off
	v_lshl_add_u64 v[10:11], v[12:13], 2, s[8:9]
	global_load_dword v10, v[10:11], off
	v_mul_f32_e32 v1, v29, v29
	v_fmac_f32_e32 v1, v28, v28
	v_fmac_f32_e32 v1, v30, v30
	v_fmac_f32_e32 v1, v31, v31
	v_max3_f32 v6, |v28|, 0, |v29|
	v_xor_b32_e32 v9, 1, v53
	v_fmac_f32_e32 v1, v32, v32
	v_max3_f32 v6, v6, |v30|, |v31|
	v_cmp_lt_i32_e32 vcc, v9, v54
	v_fmac_f32_e32 v1, v33, v33
	v_xor_b32_e32 v14, 2, v53
	v_cndmask_b32_e32 v9, v53, v9, vcc
	v_max3_f32 v6, v6, |v32|, |v33|
	v_fmac_f32_e32 v1, v34, v34
	v_cmp_lt_i32_e32 vcc, v14, v54
	v_lshlrev_b32_e32 v9, 2, v9
	v_max3_f32 v6, v6, |v34|, |v35|
	v_fmac_f32_e32 v1, v35, v35
	v_cndmask_b32_e32 v13, v53, v14, vcc
	ds_bpermute_b32 v14, v9, v6
	ds_bpermute_b32 v16, v9, v1
	v_lshlrev_b32_e32 v13, 2, v13
	v_xor_b32_e32 v11, 4, v53
	v_cmp_lt_i32_e32 vcc, v11, v54
	s_waitcnt lgkmcnt(1)
	v_max_f32_e32 v14, v14, v14
	s_waitcnt lgkmcnt(0)
	v_add_f32_e32 v1, v1, v16
	v_max_f32_e32 v6, v6, v14
	ds_bpermute_b32 v14, v13, v1
	v_cndmask_b32_e32 v11, v53, v11, vcc
	v_lshlrev_b32_e32 v11, 2, v11
	ds_bpermute_b32 v16, v13, v6
	v_xor_b32_e32 v12, 8, v53
	s_waitcnt lgkmcnt(1)
	v_add_f32_e32 v1, v1, v14
	ds_bpermute_b32 v14, v11, v1
	v_cmp_lt_i32_e32 vcc, v12, v54
	s_waitcnt lgkmcnt(1)
	v_max_f32_e32 v16, v16, v16
	v_max_f32_e32 v6, v6, v16
	v_cndmask_b32_e32 v12, v53, v12, vcc
	v_lshlrev_b32_e32 v12, 2, v12
	s_waitcnt lgkmcnt(0)
	v_add_f32_e32 v1, v1, v14
	ds_bpermute_b32 v14, v12, v1
	ds_bpermute_b32 v16, v11, v6
	s_mov_b32 s0, 0xf800000
	v_and_b32_e32 v8, 63, v0
	s_waitcnt lgkmcnt(1)
	v_add_f32_e32 v1, v1, v14
	s_waitcnt lgkmcnt(0)
	v_max_f32_e32 v16, v16, v16
	v_mul_f32_e32 v14, 0x4f800000, v1
	v_cmp_gt_f32_e32 vcc, s0, v1
	v_max_f32_e32 v6, v6, v16
	ds_bpermute_b32 v16, v12, v6
	v_cndmask_b32_e32 v1, v1, v14, vcc
	v_sqrt_f32_e32 v14, v1
	s_waitcnt vmcnt(2)
	v_fma_mix_f32 v17, v28, v2, 0 op_sel_hi:[0,1,0]
	v_fma_mix_f32 v2, v29, v2, v17 op_sel:[0,1,0] op_sel_hi:[0,1,0]
	v_fma_mix_f32 v2, v30, v3, v2 op_sel_hi:[0,1,0]
	v_fma_mix_f32 v2, v31, v3, v2 op_sel:[0,1,0] op_sel_hi:[0,1,0]
	v_fma_mix_f32 v2, v32, v4, v2 op_sel_hi:[0,1,0]
	v_fma_mix_f32 v2, v33, v4, v2 op_sel:[0,1,0] op_sel_hi:[0,1,0]
	v_fma_mix_f32 v2, v34, v5, v2 op_sel_hi:[0,1,0]
	v_fma_mix_f32 v2, v35, v5, v2 op_sel:[0,1,0] op_sel_hi:[0,1,0]
	ds_bpermute_b32 v3, v9, v2
	v_add_u32_e32 v9, -1, v14
	s_waitcnt lgkmcnt(1)
	v_max_f32_e32 v5, v16, v16
	v_add_u32_e32 v16, 1, v14
	v_fma_f32 v17, -v16, v14, v1
	s_waitcnt lgkmcnt(0)
	v_add_f32_e32 v2, v2, v3
	ds_bpermute_b32 v3, v13, v2
	v_fma_f32 v13, -v9, v14, v1
	v_cmp_ge_f32_e64 s[0:1], 0, v13
	v_mov_b32_e32 v4, 0x260
	v_max_f32_e32 v5, v6, v5
	s_waitcnt lgkmcnt(0)
	v_add_f32_e32 v2, v2, v3
	ds_bpermute_b32 v3, v11, v2
	v_cndmask_b32_e64 v9, v14, v9, s[0:1]
	v_cmp_lt_f32_e64 s[0:1], 0, v17
	s_waitcnt lgkmcnt(0)
	v_add_f32_e32 v2, v2, v3
	ds_bpermute_b32 v3, v12, v2
	v_cndmask_b32_e64 v9, v9, v16, s[0:1]
	v_mul_f32_e32 v11, 0x37800000, v9
	v_cndmask_b32_e32 v9, v9, v11, vcc
	v_cmp_class_f32_e32 vcc, v1, v4
	s_waitcnt lgkmcnt(0)
	v_add_f32_e32 v2, v2, v3
	s_waitcnt vmcnt(0)
	v_mul_f32_e32 v2, v10, v2
	v_cndmask_b32_e32 v1, v9, v1, vcc
	v_max_f32_e32 v1, 0x322bcc77, v1
	v_mul_f32_e32 v1, v15, v1
	v_div_scale_f32 v3, s[0:1], v1, v1, v2
	v_rcp_f32_e32 v4, v3
	v_div_scale_f32 v6, vcc, v2, v1, v2
	v_fma_f32 v9, -v3, v4, 1.0
	v_fmac_f32_e32 v4, v9, v4
	v_mul_f32_e32 v9, v6, v4
	v_fma_f32 v10, -v3, v9, v6
	v_fmac_f32_e32 v9, v10, v4
	v_fma_f32 v3, -v3, v9, v6
	v_div_fmas_f32 v3, v3, v4, v9
	v_div_fixup_f32 v2, v3, v1, v2
	v_mul_f32_e64 v1, v5, |v2|
	v_cndmask_b32_e64 v1, 0, v1, s[2:3]
	ds_bpermute_b32 v3, v21, v1
	v_cmp_eq_u32_e32 vcc, 0, v8
	s_waitcnt lgkmcnt(0)
	v_max_f32_e32 v3, v3, v3
	v_max_f32_e32 v3, v1, v3
	ds_bpermute_b32 v4, v52, v3
	s_and_saveexec_b64 s[0:1], vcc
	s_cbranch_execz .LBB5_38
	s_waitcnt lgkmcnt(0)
	v_max_f32_e32 v1, v4, v4
	v_max_f32_e32 v3, v3, v3
	v_max_f32_e32 v1, v3, v1
	v_lshrrev_b32_e32 v3, 4, v0
	ds_write_b32 v3, v1 offset:16384

	.amdhsa_kernel _Z6k_spmmILb1ELi1EEvPKiPK15HIP_vector_typeIiLj2EEPKvPKfPKDF16_S9_S9_iPfPDF16_PhSC_PKhS9_SG_S9_S9_i
		.amdhsa_group_segment_fixed_size 20544
		.amdhsa_private_segment_fixed_size 0
		.amdhsa_kernarg_size 400
		.amdhsa_user_sgpr_count 2
		.amdhsa_user_sgpr_dispatch_ptr 0
		.amdhsa_user_sgpr_queue_ptr 0
		.amdhsa_user_sgpr_kernarg_segment_ptr 1
		.amdhsa_user_sgpr_dispatch_id 0
		.amdhsa_user_sgpr_kernarg_preload_length 0
		.amdhsa_user_sgpr_kernarg_preload_offset 0
		.amdhsa_user_sgpr_private_segment_size 0
		.amdhsa_uses_dynamic_stack 0
		.amdhsa_enable_private_segment 0
		.amdhsa_system_sgpr_workgroup_id_x 1
		.amdhsa_system_sgpr_workgroup_id_y 0
		.amdhsa_system_sgpr_workgroup_id_z 0
		.amdhsa_system_sgpr_workgroup_info 0
		.amdhsa_system_vgpr_workitem_id 0
		.amdhsa_next_free_vgpr 64
		.amdhsa_next_free_sgpr 46
		.amdhsa_accum_offset 64
		.amdhsa_reserve_vcc 1
		.amdhsa_float_round_mode_32 0
		.amdhsa_float_round_mode_16_64 0
		.amdhsa_float_denorm_mode_32 3
		.amdhsa_float_denorm_mode_16_64 3
		.amdhsa_dx10_clamp 1
		.amdhsa_ieee_mode 1
		.amdhsa_fp16_overflow 0
		.amdhsa_tg_split 0
		.amdhsa_exception_fp_ieee_invalid_op 0
		.amdhsa_exception_fp_denorm_src 0
		.amdhsa_exception_fp_ieee_div_zero 0
		.amdhsa_exception_fp_ieee_overflow 0
		.amdhsa_exception_fp_ieee_underflow 0
		.amdhsa_exception_fp_ieee_inexact 0
		.amdhsa_exception_int_div_zero 0
	.end_amdhsa_kernel

_Z6k_spmmILb1ELi2EEvPKiPK15HIP_vector_typeIiLj2EEPKvPKfPKDF16_S9_S9_iPfPDF16_PhSC_PKhS9_SG_S9_S9_i:
	s_load_dword s3, s[0:1], 0x90
	s_load_dwordx2 s[40:41], s[0:1], 0x10
	s_load_dwordx2 s[42:43], s[0:1], 0x70
	s_load_dwordx2 s[44:45], s[0:1], 0x60
	s_load_dwordx4 s[48:51], s[0:1], 0x40
	s_load_dwordx2 s[52:53], s[0:1], 0x20
	s_load_dwordx2 s[8:9], s[0:1], 0x0
	s_load_dwordx2 s[6:7], s[0:1], 0x8
	s_load_dword s4, s[0:1], 0x38
	v_lshrrev_b32_e32 v1, 4, v0
	s_not_b32 s2, s2
	s_waitcnt lgkmcnt(0)
	s_add_i32 s16, s3, s2
	v_and_b32_e32 v2, 28, v1
	v_lshl_or_b32 v50, s16, 5, v2
	s_lshl_b32 s5, s16, 5
	s_nop 0
	v_mbcnt_lo_u32_b32 v20, -1, 0
	v_mbcnt_hi_u32_b32 v20, -1, v20
	v_min_u32_e32 v21, 32, v20
	v_add_u32_e32 v21, s5, v21
	v_min_i32_e32 v21, s4, v21
	v_lshlrev_b32_e32 v22, 2, v21
	v_lshrrev_b32_e32 v24, 6, v0
	v_lshlrev_b32_e32 v24, 9, v24
	v_lshlrev_b32_e32 v25, 2, v20
	v_add_u32_e32 v26, v24, v25
	s_waitcnt lgkmcnt(0)
	global_load_dword v23, v22, s[8:9]
	v_cmp_gt_u32_e32 vcc, 33, v20
	s_waitcnt vmcnt(0)
	s_and_saveexec_b64 s[10:11], vcc
	ds_write_b32 v26, v23 offset:16384
	s_mov_b64 exec, s[10:11]
	ds_read_b32 v27, v26 offset:16388
	v_sub_u32_e32 v28, 31, v20
	s_waitcnt lgkmcnt(0)
	v_sub_u32_e32 v27, v27, v23
	v_lshl_add_u32 v27, v27, 5, v28
	v_cmp_gt_u32_e32 vcc, 32, v20
	s_and_saveexec_b64 s[10:11], vcc
	ds_write_b32 v26, v27 offset:16544
	s_mov_b64 exec, s[10:11]
	v_mov_b32_e32 v28, 0
	ds_read_b128 v[30:33], v24 offset:16544
	s_waitcnt lgkmcnt(0)
	v_sub_u32_e32 v21, v27, v30
	v_ashrrev_i32_e32 v21, 31, v21
	v_sub_u32_e32 v28, v28, v21
	v_sub_u32_e32 v21, v27, v31
	v_ashrrev_i32_e32 v21, 31, v21
	v_sub_u32_e32 v28, v28, v21
	v_sub_u32_e32 v21, v27, v32
	v_ashrrev_i32_e32 v21, 31, v21
	v_sub_u32_e32 v28, v28, v21
	v_sub_u32_e32 v21, v27, v33
	v_ashrrev_i32_e32 v21, 31, v21
	v_sub_u32_e32 v28, v28, v21
	ds_read_b128 v[30:33], v24 offset:16560
	s_waitcnt lgkmcnt(0)
	v_sub_u32_e32 v21, v27, v30
	v_ashrrev_i32_e32 v21, 31, v21
	v_sub_u32_e32 v28, v28, v21
	v_sub_u32_e32 v21, v27, v31
	v_ashrrev_i32_e32 v21, 31, v21
	v_sub_u32_e32 v28, v28, v21
	v_sub_u32_e32 v21, v27, v32
	v_ashrrev_i32_e32 v21, 31, v21
	v_sub_u32_e32 v28, v28, v21
	v_sub_u32_e32 v21, v27, v33
	v_ashrrev_i32_e32 v21, 31, v21
	v_sub_u32_e32 v28, v28, v21
	ds_read_b128 v[30:33], v24 offset:16576
	s_waitcnt lgkmcnt(0)
	v_sub_u32_e32 v21, v27, v30
	v_ashrrev_i32_e32 v21, 31, v21
	v_sub_u32_e32 v28, v28, v21
	v_sub_u32_e32 v21, v27, v31
	v_ashrrev_i32_e32 v21, 31, v21
	v_sub_u32_e32 v28, v28, v21
	v_sub_u32_e32 v21, v27, v32
	v_ashrrev_i32_e32 v21, 31, v21
	v_sub_u32_e32 v28, v28, v21
	v_sub_u32_e32 v21, v27, v33
	v_ashrrev_i32_e32 v21, 31, v21
	v_sub_u32_e32 v28, v28, v21
	ds_read_b128 v[30:33], v24 offset:16592
	s_waitcnt lgkmcnt(0)
	v_sub_u32_e32 v21, v27, v30
	v_ashrrev_i32_e32 v21, 31, v21
	v_sub_u32_e32 v28, v28, v21
	v_sub_u32_e32 v21, v27, v31
	v_ashrrev_i32_e32 v21, 31, v21
	v_sub_u32_e32 v28, v28, v21
	v_sub_u32_e32 v21, v27, v32
	v_ashrrev_i32_e32 v21, 31, v21
	v_sub_u32_e32 v28, v28, v21
	v_sub_u32_e32 v21, v27, v33
	v_ashrrev_i32_e32 v21, 31, v21
	v_sub_u32_e32 v28, v28, v21
	ds_read_b128 v[30:33], v24 offset:16608
	s_waitcnt lgkmcnt(0)
	v_sub_u32_e32 v21, v27, v30
	v_ashrrev_i32_e32 v21, 31, v21
	v_sub_u32_e32 v28, v28, v21
	v_sub_u32_e32 v21, v27, v31
	v_ashrrev_i32_e32 v21, 31, v21
	v_sub_u32_e32 v28, v28, v21
	v_sub_u32_e32 v21, v27, v32
	v_ashrrev_i32_e32 v21, 31, v21
	v_sub_u32_e32 v28, v28, v21
	v_sub_u32_e32 v21, v27, v33
	v_ashrrev_i32_e32 v21, 31, v21
	v_sub_u32_e32 v28, v28, v21
	ds_read_b128 v[30:33], v24 offset:16624
	s_waitcnt lgkmcnt(0)
	v_sub_u32_e32 v21, v27, v30
	v_ashrrev_i32_e32 v21, 31, v21
	v_sub_u32_e32 v28, v28, v21
	v_sub_u32_e32 v21, v27, v31
	v_ashrrev_i32_e32 v21, 31, v21
	v_sub_u32_e32 v28, v28, v21
	v_sub_u32_e32 v21, v27, v32
	v_ashrrev_i32_e32 v21, 31, v21
	v_sub_u32_e32 v28, v28, v21
	v_sub_u32_e32 v21, v27, v33
	v_ashrrev_i32_e32 v21, 31, v21
	v_sub_u32_e32 v28, v28, v21
	ds_read_b128 v[30:33], v24 offset:16640
	s_waitcnt lgkmcnt(0)
	v_sub_u32_e32 v21, v27, v30
	v_ashrrev_i32_e32 v21, 31, v21
	v_sub_u32_e32 v28, v28, v21
	v_sub_u32_e32 v21, v27, v31
	v_ashrrev_i32_e32 v21, 31, v21
	v_sub_u32_e32 v28, v28, v21
	v_sub_u32_e32 v21, v27, v32
	v_ashrrev_i32_e32 v21, 31, v21
	v_sub_u32_e32 v28, v28, v21
	v_sub_u32_e32 v21, v27, v33
	v_ashrrev_i32_e32 v21, 31, v21
	v_sub_u32_e32 v28, v28, v21
	ds_read_b128 v[30:33], v24 offset:16656
	s_waitcnt lgkmcnt(0)
	v_sub_u32_e32 v21, v27, v30
	v_ashrrev_i32_e32 v21, 31, v21
	v_sub_u32_e32 v28, v28, v21
	v_sub_u32_e32 v21, v27, v31
	v_ashrrev_i32_e32 v21, 31, v21
	v_sub_u32_e32 v28, v28, v21
	v_sub_u32_e32 v21, v27, v32
	v_ashrrev_i32_e32 v21, 31, v21
	v_sub_u32_e32 v28, v28, v21
	v_sub_u32_e32 v21, v27, v33
	v_ashrrev_i32_e32 v21, 31, v21
	v_sub_u32_e32 v28, v28, v21
	v_lshl_add_u32 v21, v28, 2, v24
	v_cmp_gt_u32_e32 vcc, 32, v20
	s_and_saveexec_b64 s[10:11], vcc
	ds_write_b32 v21, v20 offset:16704
	s_mov_b64 exec, s[10:11]
	v_bfe_u32 v21, v0, 4, 5
	v_lshl_add_u32 v21, v21, 2, v24
	ds_read_b32 v22, v21 offset:16704
	s_waitcnt lgkmcnt(0)
	v_add_u32_e32 v16, s5, v22
	v_lshl_add_u32 v22, v22, 2, v24
	ds_read_b32 v4, v22 offset:16384
	ds_read_b32 v21, v22 offset:16388
	v_ashrrev_i32_e32 v17, 31, v16
	s_waitcnt lgkmcnt(0)
	v_sub_u32_e32 v52, v21, v4
	v_cmp_gt_i32_e32 vcc, s4, v16
	s_mov_b64 s[2:3], exec
	s_nop 1
	v_cndmask_b32_e32 v4, 0, v4, vcc
	v_cndmask_b32_e32 v52, 0, v52, vcc

.LBB6_10:
	s_or_b64 exec, exec, s[4:5]
	s_waitcnt vmcnt(0)
	v_ashrrev_i32_e32 v12, 5, v2
	v_ashrrev_i32_e32 v13, 31, v12
	v_ashrrev_i32_e32 v14, 5, v6
	v_ashrrev_i32_e32 v22, 5, v4
	v_ashrrev_i32_e32 v24, 5, v8
	s_waitcnt lgkmcnt(0)
	v_lshl_add_u64 v[12:13], v[12:13], 2, s[20:21]
	v_ashrrev_i32_e32 v15, 31, v14
	v_ashrrev_i32_e32 v23, 31, v22
	v_ashrrev_i32_e32 v25, 31, v24
	v_lshl_add_u64 v[14:15], v[14:15], 2, s[20:21]
	v_lshl_add_u64 v[22:23], v[22:23], 2, s[20:21]
	v_lshl_add_u64 v[24:25], v[24:25], 2, s[20:21]
	global_load_dword v11, v[12:13], off
	global_load_dword v32, v[14:15], off
	global_load_dword v34, v[22:23], off
	global_load_dword v35, v[24:25], off
	s_load_dwordx4 s[8:11], s[0:1], 0x78
	s_load_dwordx2 s[18:19], s[0:1], 0x68
	s_load_dwordx4 s[12:15], s[0:1], 0x28
	v_lshlrev_b32_e32 v0, 5, v0
	v_max_i32_e32 v21, v1, v10
	v_lshlrev_b32_e32 v18, 3, v53
	v_and_b32_e32 v54, 0x3e00, v0
	v_mov_b32_e32 v28, 0
	v_mov_b32_e32 v27, 0
	v_mov_b32_e32 v26, 0
	v_mov_b32_e32 v31, 0
	v_mov_b32_e32 v30, 0
	v_mov_b32_e32 v33, 0
	v_cmp_lt_i32_e64 s[2:3], 0, v21
	v_or_b32_e32 v55, v54, v18
	s_waitcnt vmcnt(3)
	v_mul_f32_e32 v3, v3, v11
	s_waitcnt vmcnt(2)
	v_mul_f32_e32 v7, v7, v32
	v_mov_b32_e32 v32, 0
	s_waitcnt vmcnt(1)
	v_mul_f32_e32 v5, v5, v34
	s_waitcnt vmcnt(0)
	v_mul_f32_e32 v9, v9, v35
	ds_write2_b64 v55, v[2:3], v[6:7] offset1:16
	ds_write2_b64 v55, v[4:5], v[8:9] offset0:32 offset1:48
	s_and_saveexec_b64 s[22:23], s[2:3]
	s_cbranch_execz .LBB6_36
	ds_read_b128 v[12:15], v54
	ds_read_b128 v[8:11], v54 offset:16
	s_mov_b64 s[24:25], s[40:41]
	v_cmp_lt_u32_e64 s[2:3], 8, v21
	s_waitcnt lgkmcnt(0)
	v_lshl_or_b32 v0, v12, 7, v18
	global_load_dwordx2 v[36:37], v0, s[24:25]
	v_lshl_or_b32 v0, v14, 7, v18
	global_load_dwordx2 v[34:35], v0, s[24:25]
	v_lshl_or_b32 v0, v8, 7, v18
	global_load_dwordx2 v[32:33], v0, s[24:25]
	v_lshl_or_b32 v0, v10, 7, v18
	global_load_dwordx2 v[28:29], v0, s[24:25]
	ds_read_b128 v[4:7], v54 offset:32
	ds_read_b128 v[0:3], v54 offset:48
	s_waitcnt lgkmcnt(1)
	v_lshl_or_b32 v10, v4, 7, v18
	global_load_dwordx2 v[30:31], v10, s[24:25]
	v_lshl_or_b32 v6, v6, 7, v18
	s_waitcnt lgkmcnt(0)
	v_lshl_or_b32 v2, v2, 7, v18
	global_load_dwordx2 v[26:27], v6, s[24:25]
	global_load_dwordx2 v[22:23], v2, s[24:25]
	v_lshl_or_b32 v6, v0, 7, v18
	global_load_dwordx2 v[24:25], v6, s[24:25]
	v_mov_b32_e32 v6, v15
	v_mov_b32_e32 v10, v7
	v_mov_b32_e32 v2, v11
	v_mov_b32_e32 v14, v3
	s_waitcnt vmcnt(7)
	v_cvt_pk_f32_fp8_e32 v[38:39], v36
	v_cvt_pk_f32_fp8_sdwa v[40:41], v36 src0_sel:WORD_1
	v_cvt_pk_f32_fp8_e32 v[42:43], v37
	v_cvt_pk_f32_fp8_sdwa v[36:37], v37 src0_sel:WORD_1
	s_waitcnt vmcnt(6)
	v_cvt_pk_f32_fp8_e32 v[44:45], v34
	v_cvt_pk_f32_fp8_sdwa v[46:47], v34 src0_sel:WORD_1
	v_cvt_pk_f32_fp8_e32 v[48:49], v35
	v_cvt_pk_f32_fp8_sdwa v[34:35], v35 src0_sel:WORD_1
	s_waitcnt vmcnt(5)
	v_cvt_pk_f32_fp8_e32 v[56:57], v32
	v_cvt_pk_f32_fp8_sdwa v[58:59], v32 src0_sel:WORD_1
	v_pk_fma_f32 v[38:39], v[38:39], v[12:13], 0 op_sel:[0,1,0] op_sel_hi:[1,1,0]
	v_pk_fma_f32 v[40:41], v[40:41], v[12:13], 0 op_sel:[0,1,0] op_sel_hi:[1,1,0]
	v_pk_fma_f32 v[42:43], v[42:43], v[12:13], 0 op_sel:[0,1,0] op_sel_hi:[1,1,0]
	v_pk_fma_f32 v[12:13], v[36:37], v[12:13], 0 op_sel:[0,1,0] op_sel_hi:[1,1,0]
	v_cvt_pk_f32_fp8_e32 v[36:37], v33
	v_cvt_pk_f32_fp8_sdwa v[32:33], v33 src0_sel:WORD_1
	s_waitcnt vmcnt(4)
	v_cvt_pk_f32_fp8_e32 v[60:61], v28
	v_pk_fma_f32 v[38:39], v[44:45], v[6:7], v[38:39] op_sel_hi:[1,0,1]
	v_cvt_pk_f32_fp8_sdwa v[44:45], v28 src0_sel:WORD_1
	v_pk_fma_f32 v[40:41], v[46:47], v[6:7], v[40:41] op_sel_hi:[1,0,1]
	v_cvt_pk_f32_fp8_e32 v[46:47], v29
	v_cvt_pk_f32_fp8_sdwa v[28:29], v29 src0_sel:WORD_1
	v_pk_fma_f32 v[42:43], v[48:49], v[6:7], v[42:43] op_sel_hi:[1,0,1]
	s_waitcnt vmcnt(3)
	v_cvt_pk_f32_fp8_e32 v[48:49], v30
	v_pk_fma_f32 v[6:7], v[34:35], v[6:7], v[12:13] op_sel_hi:[1,0,1]
	v_cvt_pk_f32_fp8_sdwa v[12:13], v30 src0_sel:WORD_1
	v_cvt_pk_f32_fp8_e32 v[34:35], v31
	v_cvt_pk_f32_fp8_sdwa v[30:31], v31 src0_sel:WORD_1
	v_pk_fma_f32 v[38:39], v[56:57], v[8:9], v[38:39] op_sel:[0,1,0]
	s_waitcnt vmcnt(2)
	v_cvt_pk_f32_fp8_e32 v[56:57], v26
	v_pk_fma_f32 v[40:41], v[58:59], v[8:9], v[40:41] op_sel:[0,1,0]
	v_cvt_pk_f32_fp8_sdwa v[58:59], v26 src0_sel:WORD_1
	v_pk_fma_f32 v[36:37], v[36:37], v[8:9], v[42:43] op_sel:[0,1,0]
	v_cvt_pk_f32_fp8_e32 v[42:43], v27
	v_cvt_pk_f32_fp8_sdwa v[26:27], v27 src0_sel:WORD_1
	v_pk_fma_f32 v[6:7], v[32:33], v[8:9], v[6:7] op_sel:[0,1,0]
	s_waitcnt vmcnt(0)
	v_cvt_pk_f32_fp8_e32 v[8:9], v24
	v_cvt_pk_f32_fp8_sdwa v[32:33], v24 src0_sel:WORD_1
	v_cvt_pk_f32_fp8_e32 v[62:63], v25
	v_cvt_pk_f32_fp8_sdwa v[24:25], v25 src0_sel:WORD_1
	v_pk_fma_f32 v[38:39], v[60:61], v[2:3], v[38:39] op_sel_hi:[1,0,1]
	v_cvt_pk_f32_fp8_e32 v[60:61], v22
	v_pk_fma_f32 v[40:41], v[44:45], v[2:3], v[40:41] op_sel_hi:[1,0,1]
	v_cvt_pk_f32_fp8_sdwa v[44:45], v22 src0_sel:WORD_1
	v_pk_fma_f32 v[36:37], v[46:47], v[2:3], v[36:37] op_sel_hi:[1,0,1]
	v_cvt_pk_f32_fp8_e32 v[46:47], v23
	v_cvt_pk_f32_fp8_sdwa v[22:23], v23 src0_sel:WORD_1
	v_pk_fma_f32 v[2:3], v[28:29], v[2:3], v[6:7] op_sel_hi:[1,0,1]
	v_pk_fma_f32 v[6:7], v[48:49], v[4:5], v[38:39] op_sel:[0,1,0]
	v_pk_fma_f32 v[12:13], v[12:13], v[4:5], v[40:41] op_sel:[0,1,0]
	v_pk_fma_f32 v[28:29], v[34:35], v[4:5], v[36:37] op_sel:[0,1,0]
	v_pk_fma_f32 v[2:3], v[30:31], v[4:5], v[2:3] op_sel:[0,1,0]
	v_pk_fma_f32 v[4:5], v[56:57], v[10:11], v[6:7] op_sel_hi:[1,0,1]
	v_pk_fma_f32 v[6:7], v[58:59], v[10:11], v[12:13] op_sel_hi:[1,0,1]
	v_pk_fma_f32 v[12:13], v[42:43], v[10:11], v[28:29] op_sel_hi:[1,0,1]
	v_pk_fma_f32 v[2:3], v[26:27], v[10:11], v[2:3] op_sel_hi:[1,0,1]
	v_pk_fma_f32 v[4:5], v[8:9], v[0:1], v[4:5] op_sel:[0,1,0]
	v_pk_fma_f32 v[6:7], v[32:33], v[0:1], v[6:7] op_sel:[0,1,0]
	v_pk_fma_f32 v[8:9], v[62:63], v[0:1], v[12:13] op_sel:[0,1,0]
	v_pk_fma_f32 v[0:1], v[24:25], v[0:1], v[2:3] op_sel:[0,1,0]
	v_pk_fma_f32 v[32:33], v[60:61], v[14:15], v[4:5] op_sel_hi:[1,0,1]
	v_pk_fma_f32 v[30:31], v[44:45], v[14:15], v[6:7] op_sel_hi:[1,0,1]
	v_pk_fma_f32 v[26:27], v[46:47], v[14:15], v[8:9] op_sel_hi:[1,0,1]
	v_pk_fma_f32 v[28:29], v[22:23], v[14:15], v[0:1] op_sel_hi:[1,0,1]
	s_and_saveexec_b64 s[4:5], s[2:3]
	s_cbranch_execnz .LBB6_15
	s_or_b64 exec, exec, s[4:5]
	v_cmp_lt_u32_e64 s[2:3], 16, v21
	s_and_saveexec_b64 s[4:5], s[2:3]
	s_cbranch_execnz .LBB6_16

.LBB6_36:
	s_or_b64 exec, exec, s[22:23]
	s_mov_b64 s[2:3], s[42:43]
	s_mov_b64 s[20:21], s[44:45]
	s_mov_b64 s[4:5], s[48:49]
	s_mov_b64 s[6:7], s[50:51]
	s_mov_b64 s[22:23], s[52:53]
	v_cndmask_b32_e32 v8, 0, v16, vcc
	v_ashrrev_i32_e32 v9, 31, v8
	v_lshlrev_b64 v[0:1], 8, v[8:9]
	v_mov_b32_e32 v5, 0
	s_waitcnt lgkmcnt(0)
	v_lshl_add_u64 v[0:1], s[22:23], 0, v[0:1]
	v_lshlrev_b32_e32 v4, 1, v18
	v_lshl_add_u64 v[0:1], v[0:1], 0, v[4:5]
	global_load_dwordx4 v[0:3], v[0:1], off
	v_mul_f32_e32 v4, v33, v33
	v_fmac_f32_e32 v4, v32, v32
	v_fmac_f32_e32 v4, v30, v30
	v_fmac_f32_e32 v4, v31, v31
	v_xor_b32_e32 v6, 1, v19
	v_fmac_f32_e32 v4, v26, v26
	v_cmp_lt_i32_e64 s[0:1], v6, v51
	v_fmac_f32_e32 v4, v27, v27
	v_fmac_f32_e32 v4, v28, v28
	v_cndmask_b32_e64 v6, v19, v6, s[0:1]
	v_lshlrev_b32_e32 v6, 2, v6
	v_fmac_f32_e32 v4, v29, v29
	ds_bpermute_b32 v12, v6, v4
	v_xor_b32_e32 v7, 2, v19
	v_cmp_lt_i32_e64 s[0:1], v7, v51
	v_xor_b32_e32 v10, 4, v19
	v_xor_b32_e32 v11, 8, v19
	s_waitcnt vmcnt(0)
	v_fma_mix_f32 v13, v32, v0, 0 op_sel_hi:[0,1,0]
	v_fma_mix_f32 v0, v33, v0, v13 op_sel:[0,1,0] op_sel_hi:[0,1,0]
	v_fma_mix_f32 v0, v30, v1, v0 op_sel_hi:[0,1,0]
	v_fma_mix_f32 v0, v31, v1, v0 op_sel:[0,1,0] op_sel_hi:[0,1,0]
	v_fma_mix_f32 v0, v26, v2, v0 op_sel_hi:[0,1,0]
	v_fma_mix_f32 v0, v27, v2, v0 op_sel:[0,1,0] op_sel_hi:[0,1,0]
	v_fma_mix_f32 v0, v28, v3, v0 op_sel_hi:[0,1,0]
	v_fma_mix_f32 v0, v29, v3, v0 op_sel:[0,1,0] op_sel_hi:[0,1,0]
	ds_bpermute_b32 v1, v6, v0
	v_cndmask_b32_e64 v2, v19, v7, s[0:1]
	v_lshlrev_b32_e32 v2, 2, v2
	s_waitcnt lgkmcnt(1)
	v_add_f32_e32 v3, v4, v12
	ds_bpermute_b32 v4, v2, v3
	s_waitcnt lgkmcnt(1)
	v_add_f32_e32 v0, v0, v1
	ds_bpermute_b32 v1, v2, v0
	v_cmp_lt_i32_e64 s[0:1], v10, v51
	s_waitcnt lgkmcnt(1)
	v_add_f32_e32 v3, v3, v4
	v_cndmask_b32_e64 v2, v19, v10, s[0:1]
	v_lshlrev_b32_e32 v2, 2, v2
	s_waitcnt lgkmcnt(0)
	v_add_f32_e32 v0, v0, v1
	ds_bpermute_b32 v4, v2, v3
	ds_bpermute_b32 v1, v2, v0
	v_cmp_lt_i32_e64 s[0:1], v11, v51
	s_waitcnt lgkmcnt(1)
	v_add_f32_e32 v10, v3, v4
	v_cndmask_b32_e64 v2, v19, v11, s[0:1]
	v_lshlrev_b32_e32 v2, 2, v2
	s_waitcnt lgkmcnt(0)
	v_add_f32_e32 v11, v0, v1
	ds_bpermute_b32 v12, v2, v11
	ds_bpermute_b32 v13, v2, v10
	s_and_saveexec_b64 s[0:1], vcc
	s_cbranch_execz .LBB6_38
	v_ashrrev_i32_e32 v0, 5, v50
	v_ashrrev_i32_e32 v1, 31, v0
	v_lshl_add_u64 v[0:1], v[0:1], 2, s[12:13]
	global_load_dword v6, v[0:1], off
	v_lshl_add_u64 v[0:1], v[8:9], 2, s[14:15]
	global_load_dword v7, v[0:1], off
	v_lshlrev_b64 v[0:1], 7, v[16:17]
	v_mov_b32_e32 v19, v5
	v_lshl_add_u64 v[2:3], s[20:21], 0, v[0:1]
	v_lshl_add_u64 v[2:3], v[2:3], 0, v[18:19]
	global_load_dwordx2 v[14:15], v[2:3], off
	v_lshl_add_u64 v[0:1], s[2:3], 0, v[0:1]
	v_lshlrev_b64 v[2:3], 8, v[16:17]
	v_lshl_add_u64 v[0:1], v[0:1], 0, v[18:19]
	global_load_dwordx2 v[20:21], v[0:1], off
	v_lshl_add_u64 v[0:1], s[6:7], 0, v[2:3]
	v_lshlrev_b32_e32 v4, 1, v18
	v_lshl_add_u64 v[0:1], v[0:1], 0, v[4:5]
	global_load_dwordx4 v[0:3], v[0:1], off
	s_waitcnt lgkmcnt(0)
	v_add_f32_e32 v4, v10, v13
	s_mov_b32 s2, 0xf800000
	s_ashr_i32 s17, s16, 31
	v_mul_f32_e32 v13, 0x4f800000, v4
	v_cmp_gt_f32_e32 vcc, s2, v4
	s_lshl_b64 s[0:1], s[16:17], 2
	s_add_u32 s2, s10, s0
	v_cndmask_b32_e32 v13, v4, v13, vcc
	v_sqrt_f32_e32 v4, v13
	v_lshlrev_b64 v[8:9], 9, v[16:17]
	s_addc_u32 s3, s11, s1
	v_lshl_add_u64 v[8:9], s[4:5], 0, v[8:9]
	s_load_dword s5, s[2:3], 0x0
	s_add_u32 s2, s18, s0
	s_addc_u32 s3, s19, s1
	s_add_u32 s0, s8, s0
	v_add_u32_e32 v16, -1, v4
	v_add_u32_e32 v17, 1, v4
	s_addc_u32 s1, s9, s1
	v_fma_f32 v19, -v16, v4, v13
	s_load_dword s4, s[2:3], 0x0
	v_fma_f32 v22, -v17, v4, v13
	s_load_dword s2, s[0:1], 0x0
	v_cmp_ge_f32_e64 s[0:1], 0, v19
	v_add_f32_e32 v12, v11, v12
	v_mov_b32_e32 v11, 0x43800000
	v_cndmask_b32_e64 v16, v4, v16, s[0:1]
	v_cmp_lt_f32_e64 s[0:1], 0, v22
	s_waitcnt lgkmcnt(0)
	v_mul_f32_e32 v4, s5, v11
	v_mov_b32_e32 v10, 0x260
	v_cndmask_b32_e64 v11, v16, v17, s[0:1]
	v_mul_f32_e32 v16, 0x37800000, v11
	v_cndmask_b32_e32 v11, v11, v16, vcc
	v_cmp_class_f32_e32 vcc, v13, v10
	s_waitcnt vmcnt(2)
	v_cvt_pk_f32_fp8_e32 v[22:23], v14
	v_cndmask_b32_e32 v10, v11, v13, vcc
	v_max_f32_e32 v13, 0x322bcc77, v10
	v_pk_mul_f32 v[10:11], v[6:7], v[12:13]
	v_cvt_pk_f32_fp8_e32 v[34:35], v15
	v_div_scale_f32 v19, s[0:1], v11, v11, v10
	v_rcp_f32_e32 v45, v19
	v_cvt_pk_f32_fp8_sdwa v[24:25], v14 src0_sel:WORD_1
	v_cvt_pk_f32_fp8_sdwa v[36:37], v15 src0_sel:WORD_1
	s_waitcnt vmcnt(1)
	v_cvt_pk_f32_fp8_e32 v[12:13], v20
	v_cvt_pk_f32_fp8_sdwa v[14:15], v20 src0_sel:WORD_1
	v_cvt_pk_f32_fp8_e32 v[16:17], v21
	v_cvt_pk_f32_fp8_sdwa v[6:7], v21 src0_sel:WORD_1
	s_waitcnt vmcnt(0)
	v_cvt_f32_f16_e32 v20, v0
	v_cvt_f32_f16_sdwa v21, v0 dst_sel:DWORD dst_unused:UNUSED_PAD src0_sel:WORD_1
	v_cvt_f32_f16_e32 v38, v1
	v_cvt_f32_f16_sdwa v39, v1 dst_sel:DWORD dst_unused:UNUSED_PAD src0_sel:WORD_1
	v_pk_mul_f32 v[0:1], s[4:5], v[22:23] op_sel_hi:[0,1]
	v_pk_mul_f32 v[22:23], s[4:5], v[34:35] op_sel_hi:[0,1]
	v_fma_f32 v34, -v19, v45, 1.0
	v_div_scale_f32 v44, vcc, v10, v11, v10
	v_fmac_f32_e32 v45, v34, v45
	v_mul_f32_e32 v34, v44, v45
	v_fma_f32 v35, -v19, v34, v44
	v_fmac_f32_e32 v34, v35, v45
	v_fma_f32 v19, -v19, v34, v44
	v_cvt_f32_f16_e32 v40, v2
	v_cvt_f32_f16_sdwa v41, v2 dst_sel:DWORD dst_unused:UNUSED_PAD src0_sel:WORD_1
	v_cvt_f32_f16_e32 v42, v3
	v_cvt_f32_f16_sdwa v43, v3 dst_sel:DWORD dst_unused:UNUSED_PAD src0_sel:WORD_1
	v_div_fmas_f32 v19, v19, v45, v34
	v_pk_mul_f32 v[2:3], s[4:5], v[24:25] op_sel_hi:[0,1]
	v_pk_mul_f32 v[24:25], s[4:5], v[36:37] op_sel_hi:[0,1]
	v_div_fixup_f32 v10, v19, v11, v10
	v_pk_fma_f32 v[0:1], v[10:11], v[32:33], v[0:1] op_sel_hi:[0,1,1]
	v_pk_fma_f32 v[2:3], v[10:11], v[30:31], v[2:3] op_sel_hi:[0,1,1]
	v_pk_fma_f32 v[22:23], v[10:11], v[26:27], v[22:23] op_sel_hi:[0,1,1]
	v_pk_fma_f32 v[24:25], v[10:11], v[28:29], v[24:25] op_sel_hi:[0,1,1]
	v_pk_fma_f32 v[0:1], s[2:3], v[12:13], v[0:1] op_sel_hi:[0,1,1]
	v_pk_fma_f32 v[2:3], s[2:3], v[14:15], v[2:3] op_sel_hi:[0,1,1]
	v_pk_fma_f32 v[10:11], s[2:3], v[16:17], v[22:23] op_sel_hi:[0,1,1]
	v_pk_fma_f32 v[6:7], s[2:3], v[6:7], v[24:25] op_sel_hi:[0,1,1]
	v_pk_fma_f32 v[0:1], v[4:5], v[20:21], v[0:1] op_sel_hi:[0,1,1]
	v_pk_fma_f32 v[2:3], v[4:5], v[38:39], v[2:3] op_sel_hi:[0,1,1]
	v_pk_fma_f32 v[10:11], v[4:5], v[40:41], v[10:11] op_sel_hi:[0,1,1]
	v_pk_fma_f32 v[12:13], v[4:5], v[42:43], v[6:7] op_sel_hi:[0,1,1]
	v_lshlrev_b32_e32 v4, 2, v18
	v_lshl_add_u64 v[4:5], v[8:9], 0, v[4:5]
	global_store_dwordx4 v[4:5], v[0:3], off nt
	global_store_dwordx4 v[4:5], v[10:13], off offset:16 nt

	.amdhsa_kernel _Z6k_spmmILb1ELi2EEvPKiPK15HIP_vector_typeIiLj2EEPKvPKfPKDF16_S9_S9_iPfPDF16_PhSC_PKhS9_SG_S9_S9_i
		.amdhsa_group_segment_fixed_size 20480
		.amdhsa_private_segment_fixed_size 0
		.amdhsa_kernarg_size 400
		.amdhsa_user_sgpr_count 2
		.amdhsa_user_sgpr_dispatch_ptr 0
		.amdhsa_user_sgpr_queue_ptr 0
		.amdhsa_user_sgpr_kernarg_segment_ptr 1
		.amdhsa_user_sgpr_dispatch_id 0
		.amdhsa_user_sgpr_kernarg_preload_length 0
		.amdhsa_user_sgpr_kernarg_preload_offset 0
		.amdhsa_user_sgpr_private_segment_size 0
		.amdhsa_uses_dynamic_stack 0
		.amdhsa_enable_private_segment 0
		.amdhsa_system_sgpr_workgroup_id_x 1
		.amdhsa_system_sgpr_workgroup_id_y 0
		.amdhsa_system_sgpr_workgroup_id_z 0
		.amdhsa_system_sgpr_workgroup_info 0
		.amdhsa_system_vgpr_workitem_id 0
		.amdhsa_next_free_vgpr 64
		.amdhsa_next_free_sgpr 54
		.amdhsa_accum_offset 64
		.amdhsa_reserve_vcc 1
		.amdhsa_float_round_mode_32 0
		.amdhsa_float_round_mode_16_64 0
		.amdhsa_float_denorm_mode_32 3
		.amdhsa_float_denorm_mode_16_64 3
		.amdhsa_dx10_clamp 1
		.amdhsa_ieee_mode 1
		.amdhsa_fp16_overflow 0
		.amdhsa_tg_split 0
		.amdhsa_exception_fp_ieee_invalid_op 0
		.amdhsa_exception_fp_denorm_src 0
		.amdhsa_exception_fp_ieee_div_zero 0
		.amdhsa_exception_fp_ieee_overflow 0
		.amdhsa_exception_fp_ieee_underflow 0
		.amdhsa_exception_fp_ieee_inexact 0
		.amdhsa_exception_int_div_zero 0
	.end_amdhsa_kernel

amdhsa.kernels:
  - .agpr_count:     0
    .args:
      - .actual_access:  read_only
        .address_space:  global
        .offset:         0
        .size:           8
        .value_kind:     global_buffer
      - .actual_access:  write_only
        .address_space:  global
        .offset:         8
        .size:           8
        .value_kind:     global_buffer
      - .offset:         16
        .size:           4
        .value_kind:     by_value
      - .offset:         20
        .size:           4
        .value_kind:     by_value
    .group_segment_fixed_size: 8192
    .kernarg_segment_align: 8
    .kernarg_segment_size: 24
    .language:       OpenCL C
    .language_version:
      - 2
      - 0
    .max_flat_workgroup_size: 1024
    .name:           _Z7k_bhistPKiPiii
    .private_segment_fixed_size: 0
    .sgpr_count:     24
    .sgpr_spill_count: 0
    .symbol:         _Z7k_bhistPKiPiii.kd
    .uniform_work_group_size: 1
    .uses_dynamic_stack: false
    .vgpr_count:     50
    .vgpr_spill_count: 0
    .wavefront_size: 64
  - .agpr_count:     0
    .args:
      - .address_space:  global
        .offset:         0
        .size:           8
        .value_kind:     global_buffer
      - .actual_access:  write_only
        .address_space:  global
        .offset:         8
        .size:           8
        .value_kind:     global_buffer
      - .offset:         16
        .size:           4
        .value_kind:     by_value
      - .offset:         20
        .size:           4
        .value_kind:     by_value
      - .offset:         24
        .size:           4
        .value_kind:     by_value
      - .actual_access:  read_only
        .address_space:  global
        .offset:         32
        .size:           8
        .value_kind:     global_buffer
      - .actual_access:  read_only
        .address_space:  global
        .offset:         40
        .size:           8
        .value_kind:     global_buffer
      - .offset:         48
        .size:           4
        .value_kind:     by_value
      - .offset:         52
        .size:           4
        .value_kind:     by_value
      - .actual_access:  write_only
        .address_space:  global
        .offset:         56
        .size:           8
        .value_kind:     global_buffer
      - .actual_access:  write_only
        .address_space:  global
        .offset:         64
        .size:           8
        .value_kind:     global_buffer
      - .actual_access:  write_only
        .address_space:  global
        .offset:         72
        .size:           8
        .value_kind:     global_buffer
    .group_segment_fixed_size: 4160
    .kernarg_segment_align: 8
    .kernarg_segment_size: 80
    .language:       OpenCL C
    .language_version:
      - 2
      - 0
    .max_flat_workgroup_size: 1024
    .name:           _Z12k_bscan_prepPiS_iiiPKfS1_iiPDF16_PfS3_
    .private_segment_fixed_size: 0
    .sgpr_count:     24
    .sgpr_spill_count: 0
    .symbol:         _Z12k_bscan_prepPiS_iiiPKfS1_iiPDF16_PfS3_.kd
    .uniform_work_group_size: 1
    .uses_dynamic_stack: false
    .vgpr_count:     28
    .vgpr_spill_count: 0
    .wavefront_size: 64
  - .agpr_count:     0
    .args:
      - .actual_access:  read_only
        .address_space:  global
        .offset:         0
        .size:           8
        .value_kind:     global_buffer
      - .actual_access:  read_only
        .address_space:  global
        .offset:         8
        .size:           8
        .value_kind:     global_buffer
      - .actual_access:  read_only
        .address_space:  global
        .offset:         16
        .size:           8
        .value_kind:     global_buffer
      - .actual_access:  read_only
        .address_space:  global
        .offset:         24
        .size:           8
        .value_kind:     global_buffer
      - .actual_access:  read_only
        .address_space:  global
        .offset:         32
        .size:           8
        .value_kind:     global_buffer
      - .actual_access:  write_only
        .address_space:  global
        .offset:         40
        .size:           8
        .value_kind:     global_buffer
      - .actual_access:  write_only
        .address_space:  global
        .offset:         48
        .size:           8
        .value_kind:     global_buffer
      - .offset:         56
        .size:           4
        .value_kind:     by_value
      - .offset:         60
        .size:           4
        .value_kind:     by_value
      - .offset:         64
        .size:           4
        .value_kind:     by_value
      - .offset:         72
        .size:           4
        .value_kind:     hidden_block_count_x
      - .offset:         76
        .size:           4
        .value_kind:     hidden_block_count_y
      - .offset:         80
        .size:           4
        .value_kind:     hidden_block_count_z
      - .offset:         84
        .size:           2
        .value_kind:     hidden_group_size_x
      - .offset:         86
        .size:           2
        .value_kind:     hidden_group_size_y
      - .offset:         88
        .size:           2
        .value_kind:     hidden_group_size_z
      - .offset:         90
        .size:           2
        .value_kind:     hidden_remainder_x
      - .offset:         92
        .size:           2
        .value_kind:     hidden_remainder_y
      - .offset:         94
        .size:           2
        .value_kind:     hidden_remainder_z
      - .offset:         112
        .size:           8
        .value_kind:     hidden_global_offset_x
      - .offset:         120
        .size:           8
        .value_kind:     hidden_global_offset_y
      - .offset:         128
        .size:           8
        .value_kind:     hidden_global_offset_z
      - .offset:         136
        .size:           2
        .value_kind:     hidden_grid_dims
    .group_segment_fixed_size: 154816
    .kernarg_segment_align: 8
    .kernarg_segment_size: 328
    .language:       OpenCL C
    .language_version:
      - 2
      - 0
    .max_flat_workgroup_size: 1024
    .name:           _Z4k_l1PKiS0_PKfS0_S0_PiP15HIP_vector_typeIiLj2EEiii
    .private_segment_fixed_size: 0
    .sgpr_count:     92
    .sgpr_spill_count: 0
    .symbol:         _Z4k_l1PKiS0_PKfS0_S0_PiP15HIP_vector_typeIiLj2EEiii.kd
    .uniform_work_group_size: 1
    .uses_dynamic_stack: false
    .vgpr_count:     128
    .vgpr_spill_count: 0
    .wavefront_size: 64
  - .agpr_count:     0
    .args:
      - .actual_access:  read_only
        .address_space:  global
        .offset:         0
        .size:           8
        .value_kind:     global_buffer
      - .actual_access:  read_only
        .address_space:  global
        .offset:         8
        .size:           8
        .value_kind:     global_buffer
      - .actual_access:  write_only
        .address_space:  global
        .offset:         16
        .size:           8
        .value_kind:     global_buffer
      - .actual_access:  write_only
        .address_space:  global
        .offset:         24
        .size:           8
        .value_kind:     global_buffer
      - .offset:         32
        .size:           4
        .value_kind:     by_value
      - .offset:         36
        .size:           4
        .value_kind:     by_value
      - .offset:         40
        .size:           4
        .value_kind:     hidden_block_count_x
      - .offset:         44
        .size:           4
        .value_kind:     hidden_block_count_y
      - .offset:         48
        .size:           4
        .value_kind:     hidden_block_count_z
      - .offset:         52
        .size:           2
        .value_kind:     hidden_group_size_x
      - .offset:         54
        .size:           2
        .value_kind:     hidden_group_size_y
      - .offset:         56
        .size:           2
        .value_kind:     hidden_group_size_z
      - .offset:         58
        .size:           2
        .value_kind:     hidden_remainder_x
      - .offset:         60
        .size:           2
        .value_kind:     hidden_remainder_y
      - .offset:         62
        .size:           2
        .value_kind:     hidden_remainder_z
      - .offset:         80
        .size:           8
        .value_kind:     hidden_global_offset_x
      - .offset:         88
        .size:           8
        .value_kind:     hidden_global_offset_y
      - .offset:         96
        .size:           8
        .value_kind:     hidden_global_offset_z
      - .offset:         104
        .size:           2
        .value_kind:     hidden_grid_dims
    .group_segment_fixed_size: 80448
    .kernarg_segment_align: 8
    .kernarg_segment_size: 296
    .language:       OpenCL C
    .language_version:
      - 2
      - 0
    .max_flat_workgroup_size: 1024
    .name:           _Z4k_l2PK15HIP_vector_typeIiLj2EEPKiPiPS0_ii
    .private_segment_fixed_size: 0
    .sgpr_count:     54
    .sgpr_spill_count: 0
    .symbol:         _Z4k_l2PK15HIP_vector_typeIiLj2EEPKiPiPS0_ii.kd
    .uniform_work_group_size: 1
    .uses_dynamic_stack: false
    .vgpr_count:     64
    .vgpr_spill_count: 0
    .wavefront_size: 64
  - .agpr_count:     0
    .args:
      - .actual_access:  read_only
        .address_space:  global
        .offset:         0
        .size:           8
        .value_kind:     global_buffer
      - .actual_access:  read_only
        .address_space:  global
        .offset:         8
        .size:           8
        .value_kind:     global_buffer
      - .actual_access:  read_only
        .address_space:  global
        .offset:         16
        .size:           8
        .value_kind:     global_buffer
      - .actual_access:  read_only
        .address_space:  global
        .offset:         24
        .size:           8
        .value_kind:     global_buffer
      - .actual_access:  read_only
        .address_space:  global
        .offset:         32
        .size:           8
        .value_kind:     global_buffer
      - .actual_access:  read_only
        .address_space:  global
        .offset:         40
        .size:           8
        .value_kind:     global_buffer
      - .actual_access:  read_only
        .address_space:  global
        .offset:         48
        .size:           8
        .value_kind:     global_buffer
      - .offset:         56
        .size:           4
        .value_kind:     by_value
      - .actual_access:  read_only
        .address_space:  global
        .offset:         64
        .size:           8
        .value_kind:     global_buffer
      - .actual_access:  write_only
        .address_space:  global
        .offset:         72
        .size:           8
        .value_kind:     global_buffer
      - .actual_access:  write_only
        .address_space:  global
        .offset:         80
        .size:           8
        .value_kind:     global_buffer
      - .actual_access:  write_only
        .address_space:  global
        .offset:         88
        .size:           8
        .value_kind:     global_buffer
      - .actual_access:  read_only
        .address_space:  global
        .offset:         96
        .size:           8
        .value_kind:     global_buffer
      - .actual_access:  read_only
        .address_space:  global
        .offset:         104
        .size:           8
        .value_kind:     global_buffer
      - .actual_access:  read_only
        .address_space:  global
        .offset:         112
        .size:           8
        .value_kind:     global_buffer
      - .actual_access:  read_only
        .address_space:  global
        .offset:         120
        .size:           8
        .value_kind:     global_buffer
      - .actual_access:  read_only
        .address_space:  global
        .offset:         128
        .size:           8
        .value_kind:     global_buffer
      - .offset:         136
        .size:           4
        .value_kind:     by_value
      - .offset:         144
        .size:           4
        .value_kind:     hidden_block_count_x
      - .offset:         148
        .size:           4
        .value_kind:     hidden_block_count_y
      - .offset:         152
        .size:           4
        .value_kind:     hidden_block_count_z
      - .offset:         156
        .size:           2
        .value_kind:     hidden_group_size_x
      - .offset:         158
        .size:           2
        .value_kind:     hidden_group_size_y
      - .offset:         160
        .size:           2
        .value_kind:     hidden_group_size_z
      - .offset:         162
        .size:           2
        .value_kind:     hidden_remainder_x
      - .offset:         164
        .size:           2
        .value_kind:     hidden_remainder_y
      - .offset:         166
        .size:           2
        .value_kind:     hidden_remainder_z
      - .offset:         184
        .size:           8
        .value_kind:     hidden_global_offset_x
      - .offset:         192
        .size:           8
        .value_kind:     hidden_global_offset_y
      - .offset:         200
        .size:           8
        .value_kind:     hidden_global_offset_z
      - .offset:         208
        .size:           2
        .value_kind:     hidden_grid_dims
    .group_segment_fixed_size: 20544
    .kernarg_segment_align: 8
    .kernarg_segment_size: 400
    .language:       OpenCL C
    .language_version:
      - 2
      - 0
    .max_flat_workgroup_size: 512
    .name:           _Z6k_spmmILb0ELi0EEvPKiPK15HIP_vector_typeIiLj2EEPKvPKfPKDF16_S9_S9_iPfPDF16_PhSC_PKhS9_SG_S9_S9_i
    .private_segment_fixed_size: 0
    .sgpr_count:     56
    .sgpr_spill_count: 0
    .symbol:         _Z6k_spmmILb0ELi0EEvPKiPK15HIP_vector_typeIiLj2EEPKvPKfPKDF16_S9_S9_iPfPDF16_PhSC_PKhS9_SG_S9_S9_i.kd
    .uniform_work_group_size: 1
    .uses_dynamic_stack: false
    .vgpr_count:     128
    .vgpr_spill_count: 0
    .wavefront_size: 64
  - .agpr_count:     0
    .args:
      - .actual_access:  read_only
        .address_space:  global
        .offset:         0
        .size:           8
        .value_kind:     global_buffer
      - .actual_access:  read_only
        .address_space:  global
        .offset:         8
        .size:           8
        .value_kind:     global_buffer
      - .actual_access:  read_only
        .address_space:  global
        .offset:         16
        .size:           8
        .value_kind:     global_buffer
      - .actual_access:  read_only
        .address_space:  global
        .offset:         24
        .size:           8
        .value_kind:     global_buffer
      - .actual_access:  read_only
        .address_space:  global
        .offset:         32
        .size:           8
        .value_kind:     global_buffer
      - .actual_access:  read_only
        .address_space:  global
        .offset:         40
        .size:           8
        .value_kind:     global_buffer
      - .actual_access:  read_only
        .address_space:  global
        .offset:         48
        .size:           8
        .value_kind:     global_buffer
      - .offset:         56
        .size:           4
        .value_kind:     by_value
      - .actual_access:  read_only
        .address_space:  global
        .offset:         64
        .size:           8
        .value_kind:     global_buffer
      - .actual_access:  read_only
        .address_space:  global
        .offset:         72
        .size:           8
        .value_kind:     global_buffer
      - .actual_access:  write_only
        .address_space:  global
        .offset:         80
        .size:           8
        .value_kind:     global_buffer
      - .actual_access:  write_only
        .address_space:  global
        .offset:         88
        .size:           8
        .value_kind:     global_buffer
      - .actual_access:  read_only
        .address_space:  global
        .offset:         96
        .size:           8
        .value_kind:     global_buffer
      - .actual_access:  read_only
        .address_space:  global
        .offset:         104
        .size:           8
        .value_kind:     global_buffer
      - .actual_access:  read_only
        .address_space:  global
        .offset:         112
        .size:           8
        .value_kind:     global_buffer
      - .actual_access:  read_only
        .address_space:  global
        .offset:         120
        .size:           8
        .value_kind:     global_buffer
      - .actual_access:  read_only
        .address_space:  global
        .offset:         128
        .size:           8
        .value_kind:     global_buffer
      - .offset:         136
        .size:           4
        .value_kind:     by_value
      - .offset:         144
        .size:           4
        .value_kind:     hidden_block_count_x
      - .offset:         148
        .size:           4
        .value_kind:     hidden_block_count_y
      - .offset:         152
        .size:           4
        .value_kind:     hidden_block_count_z
      - .offset:         156
        .size:           2
        .value_kind:     hidden_group_size_x
      - .offset:         158
        .size:           2
        .value_kind:     hidden_group_size_y
      - .offset:         160
        .size:           2
        .value_kind:     hidden_group_size_z
      - .offset:         162
        .size:           2
        .value_kind:     hidden_remainder_x
      - .offset:         164
        .size:           2
        .value_kind:     hidden_remainder_y
      - .offset:         166
        .size:           2
        .value_kind:     hidden_remainder_z
      - .offset:         184
        .size:           8
        .value_kind:     hidden_global_offset_x
      - .offset:         192
        .size:           8
        .value_kind:     hidden_global_offset_y
      - .offset:         200
        .size:           8
        .value_kind:     hidden_global_offset_z
      - .offset:         208
        .size:           2
        .value_kind:     hidden_grid_dims
    .group_segment_fixed_size: 20544
    .kernarg_segment_align: 8
    .kernarg_segment_size: 400
    .language:       OpenCL C
    .language_version:
      - 2
      - 0
    .max_flat_workgroup_size: 512
    .name:           _Z6k_spmmILb1ELi1EEvPKiPK15HIP_vector_typeIiLj2EEPKvPKfPKDF16_S9_S9_iPfPDF16_PhSC_PKhS9_SG_S9_S9_i
    .private_segment_fixed_size: 0
    .sgpr_count:     52
    .sgpr_spill_count: 0
    .symbol:         _Z6k_spmmILb1ELi1EEvPKiPK15HIP_vector_typeIiLj2EEPKvPKfPKDF16_S9_S9_iPfPDF16_PhSC_PKhS9_SG_S9_S9_i.kd
    .uniform_work_group_size: 1
    .uses_dynamic_stack: false
    .vgpr_count:     64
    .vgpr_spill_count: 0
    .wavefront_size: 64
  - .agpr_count:     0
    .args:
      - .actual_access:  read_only
        .address_space:  global
        .offset:         0
        .size:           8
        .value_kind:     global_buffer
      - .actual_access:  read_only
        .address_space:  global
        .offset:         8
        .size:           8
        .value_kind:     global_buffer
      - .actual_access:  read_only
        .address_space:  global
        .offset:         16
        .size:           8
        .value_kind:     global_buffer
      - .actual_access:  read_only
        .address_space:  global
        .offset:         24
        .size:           8
        .value_kind:     global_buffer
      - .actual_access:  read_only
        .address_space:  global
        .offset:         32
        .size:           8
        .value_kind:     global_buffer
      - .actual_access:  read_only
        .address_space:  global
        .offset:         40
        .size:           8
        .value_kind:     global_buffer
      - .actual_access:  read_only
        .address_space:  global
        .offset:         48
        .size:           8
        .value_kind:     global_buffer
      - .offset:         56
        .size:           4
        .value_kind:     by_value
      - .actual_access:  write_only
        .address_space:  global
        .offset:         64
        .size:           8
        .value_kind:     global_buffer
      - .actual_access:  read_only
        .address_space:  global
        .offset:         72
        .size:           8
        .value_kind:     global_buffer
      - .actual_access:  read_only
        .address_space:  global
        .offset:         80
        .size:           8
        .value_kind:     global_buffer
      - .actual_access:  read_only
        .address_space:  global
        .offset:         88
        .size:           8
        .value_kind:     global_buffer
      - .actual_access:  read_only
        .address_space:  global
        .offset:         96
        .size:           8
        .value_kind:     global_buffer
      - .actual_access:  read_only
        .address_space:  global
        .offset:         104
        .size:           8
        .value_kind:     global_buffer
      - .actual_access:  read_only
        .address_space:  global
        .offset:         112
        .size:           8
        .value_kind:     global_buffer
      - .actual_access:  read_only
        .address_space:  global
        .offset:         120
        .size:           8
        .value_kind:     global_buffer
      - .actual_access:  read_only
        .address_space:  global
        .offset:         128
        .size:           8
        .value_kind:     global_buffer
      - .offset:         136
        .size:           4
        .value_kind:     by_value
      - .offset:         144
        .size:           4
        .value_kind:     hidden_block_count_x
      - .offset:         148
        .size:           4
        .value_kind:     hidden_block_count_y
      - .offset:         152
        .size:           4
        .value_kind:     hidden_block_count_z
      - .offset:         156
        .size:           2
        .value_kind:     hidden_group_size_x
      - .offset:         158
        .size:           2
        .value_kind:     hidden_group_size_y
      - .offset:         160
        .size:           2
        .value_kind:     hidden_group_size_z
      - .offset:         162
        .size:           2
        .value_kind:     hidden_remainder_x
      - .offset:         164
        .size:           2
        .value_kind:     hidden_remainder_y
      - .offset:         166
        .size:           2
        .value_kind:     hidden_remainder_z
      - .offset:         184
        .size:           8
        .value_kind:     hidden_global_offset_x
      - .offset:         192
        .size:           8
        .value_kind:     hidden_global_offset_y
      - .offset:         200
        .size:           8
        .value_kind:     hidden_global_offset_z
      - .offset:         208
        .size:           2
        .value_kind:     hidden_grid_dims
    .group_segment_fixed_size: 20480
    .kernarg_segment_align: 8
    .kernarg_segment_size: 400
    .language:       OpenCL C
    .language_version:
      - 2
      - 0
    .max_flat_workgroup_size: 512
    .name:           _Z6k_spmmILb1ELi2EEvPKiPK15HIP_vector_typeIiLj2EEPKvPKfPKDF16_S9_S9_iPfPDF16_PhSC_PKhS9_SG_S9_S9_i
    .private_segment_fixed_size: 0
    .sgpr_count:     60
    .sgpr_spill_count: 0
    .symbol:         _Z6k_spmmILb1ELi2EEvPKiPK15HIP_vector_typeIiLj2EEPKvPKfPKDF16_S9_S9_iPfPDF16_PhSC_PKhS9_SG_S9_S9_i.kd
    .uniform_work_group_size: 1
    .uses_dynamic_stack: false
    .vgpr_count:     64
    .vgpr_spill_count: 0
    .wavefront_size: 64
